# gather: integer dot totals stay integer through the transposing butterfly (one cvt instead of 16), last DPP move of each round folded into its add
# speedup vs baseline: 1.0076x; 1.0076x over previous
.LBB0_763:
	s_cmpk_eq_i32 s58, 0x80
	s_cselect_b64 s[12:13], -1, 0
	ds_bpermute_b32 v84, v93, v92
	s_and_b64 vcc, s[12:13], s[48:49]
	v_cndmask_b32_e32 v104, v0, v94, vcc
	v_ashrrev_i32_e32 v105, 31, v104
	s_and_b32 s12, s58, 0x70
	v_lshlrev_b64 v[104:105], 9, v[104:105]
	v_lshl_add_u64 v[104:105], s[94:95], 0, v[104:105]
	s_lshl_b32 s36, s12, 2
	s_waitcnt lgkmcnt(0)
	v_ashrrev_i32_e32 v85, 31, v84
	v_lshl_add_u64 v[104:105], v[104:105], 0, s[36:37]
	v_lshl_add_u64 v[84:85], v[84:85], 3, s[8:9]
	v_lshl_add_u64 v[104:105], v[104:105], 0, v[144:145]
	global_load_dwordx2 v[84:85], v[84:85], off
	s_nop 0
	global_load_dword v86, v[72:73], off
	global_load_dword v92, v[104:105], off
	s_waitcnt vmcnt(11)
	v_dot8_i32_i4 v87, v8, v1, 0
	v_dot8_i32_i4 v104, v8, v88, 0
	v_dot8_i32_i4 v87, v9, v89, v87
	v_dot8_i32_i4 v104, v9, v90, v104
	s_waitcnt vmcnt(10)
	v_dot8_i32_i4 v9, v10, v88, 0
	v_dot8_i32_i4 v9, v11, v90, v9
	v_lshl_add_u32 v87, v87, 4, v104
	v_dot8_i32_i4 v8, v10, v1, 0
	v_dot8_i32_i4 v8, v11, v89, v8
	s_add_i32 s58, s58, 16
	v_lshl_add_u64 v[72:73], v[72:73], 0, 64
	s_waitcnt vmcnt(2)
	v_mul_f32_e32 v85, v91, v85
	v_lshl_add_u32 v104, v8, 4, v9
	v_dot8_i32_i4 v8, v12, v1, 0
	v_dot8_i32_i4 v9, v12, v88, 0
	v_dot8_i32_i4 v8, v13, v89, v8
	v_dot8_i32_i4 v9, v13, v90, v9
	s_waitcnt vmcnt(0)
	v_readlane_b32 s12, v92, 0
	v_readlane_b32 s28, v92, 8
	v_readlane_b32 s30, v92, 9
	v_lshl_add_u32 v105, v8, 4, v9
	v_dot8_i32_i4 v8, v14, v1, 0
	v_dot8_i32_i4 v9, v14, v88, 0
	v_dot8_i32_i4 v8, v15, v89, v8
	v_dot8_i32_i4 v9, v15, v90, v9
	s_ashr_i32 s13, s12, 31
	v_readlane_b32 s14, v92, 1
	s_ashr_i32 s29, s28, 31
	v_lshl_add_u32 v106, v8, 4, v9
	v_dot8_i32_i4 v8, v16, v1, 0
	v_dot8_i32_i4 v9, v16, v88, 0
	v_dot8_i32_i4 v8, v17, v89, v8
	v_dot8_i32_i4 v9, v17, v90, v9
	s_ashr_i32 s31, s30, 31
	v_readlane_b32 s34, v92, 10
	s_lshl_b64 s[12:13], s[12:13], 9
	v_lshl_add_u32 v107, v8, 4, v9
	v_dot8_i32_i4 v8, v18, v1, 0
	v_dot8_i32_i4 v9, v18, v88, 0
	v_dot8_i32_i4 v8, v19, v89, v8
	v_dot8_i32_i4 v9, v19, v90, v9
	s_ashr_i32 s15, s14, 31
	v_readlane_b32 s16, v92, 2
	s_lshl_b64 s[28:29], s[28:29], 9
	v_lshl_add_u32 v108, v8, 4, v9
	v_dot8_i32_i4 v8, v20, v1, 0
	v_dot8_i32_i4 v9, v20, v88, 0
	v_dot8_i32_i4 v8, v21, v89, v8
	v_dot8_i32_i4 v9, v21, v90, v9
	s_lshl_b64 s[30:31], s[30:31], 9
	s_ashr_i32 s35, s34, 31
	v_readlane_b32 s38, v92, 11
	v_lshl_add_u32 v109, v8, 4, v9
	v_dot8_i32_i4 v8, v22, v1, 0
	v_dot8_i32_i4 v9, v22, v88, 0
	v_dot8_i32_i4 v8, v23, v89, v8
	v_dot8_i32_i4 v9, v23, v90, v9
	s_lshl_b64 s[14:15], s[14:15], 9
	s_ashr_i32 s17, s16, 31
	v_readlane_b32 s18, v92, 3
	v_lshl_add_u32 v110, v8, 4, v9
	v_dot8_i32_i4 v8, v24, v1, 0
	v_dot8_i32_i4 v9, v24, v88, 0
	v_dot8_i32_i4 v8, v25, v89, v8
	v_dot8_i32_i4 v9, v25, v90, v9
	s_lshl_b64 s[34:35], s[34:35], 9
	s_ashr_i32 s39, s38, 31
	s_nop 0
	v_lshl_add_u32 v111, v8, 4, v9
	v_dot8_i32_i4 v8, v38, v1, 0
	v_dot8_i32_i4 v9, v38, v88, 0
	v_dot8_i32_i4 v8, v39, v89, v8
	v_dot8_i32_i4 v9, v39, v90, v9
	v_permlane32_swap_b32 v87, v111
	s_nop 1
	v_lshl_add_u32 v112, v8, 4, v9
	v_dot8_i32_i4 v8, v50, v1, 0
	v_dot8_i32_i4 v9, v50, v88, 0
	v_dot8_i32_i4 v8, v51, v89, v8
	v_dot8_i32_i4 v9, v51, v90, v9
	s_waitcnt lgkmcnt(0)
	v_add_u32_e32 v87, v87, v111
	v_permlane32_swap_b32 v104, v112
	v_lshl_add_u32 v113, v8, 4, v9
	v_dot8_i32_i4 v8, v48, v1, 0
	v_dot8_i32_i4 v9, v48, v88, 0
	v_dot8_i32_i4 v8, v49, v89, v8
	v_dot8_i32_i4 v9, v49, v90, v9
	s_waitcnt lgkmcnt(0)
	v_add_u32_e32 v104, v104, v112
	v_permlane32_swap_b32 v105, v113
	v_lshl_add_u32 v114, v8, 4, v9
	v_dot8_i32_i4 v8, v46, v1, 0
	v_dot8_i32_i4 v9, v46, v88, 0
	v_dot8_i32_i4 v8, v47, v89, v8
	v_dot8_i32_i4 v9, v47, v90, v9
	s_waitcnt lgkmcnt(0)
	v_add_u32_e32 v105, v105, v113
	v_permlane32_swap_b32 v106, v114
	v_lshl_add_u32 v115, v8, 4, v9
	v_dot8_i32_i4 v8, v44, v1, 0
	v_dot8_i32_i4 v9, v44, v88, 0
	v_dot8_i32_i4 v8, v45, v89, v8
	v_dot8_i32_i4 v9, v45, v90, v9
	s_waitcnt lgkmcnt(0)
	v_add_u32_e32 v106, v106, v114
	v_permlane32_swap_b32 v107, v115
	v_lshl_add_u32 v116, v8, 4, v9
	v_dot8_i32_i4 v8, v42, v1, 0
	v_dot8_i32_i4 v9, v42, v88, 0
	v_dot8_i32_i4 v8, v43, v89, v8
	v_dot8_i32_i4 v9, v43, v90, v9
	s_waitcnt lgkmcnt(0)
	v_add_u32_e32 v107, v107, v115
	v_permlane32_swap_b32 v108, v116
	v_lshl_add_u32 v117, v8, 4, v9
	v_dot8_i32_i4 v8, v40, v1, 0
	v_dot8_i32_i4 v9, v40, v88, 0
	v_dot8_i32_i4 v8, v41, v89, v8
	v_dot8_i32_i4 v9, v41, v90, v9
	s_waitcnt lgkmcnt(0)
	v_add_u32_e32 v108, v108, v116
	v_permlane32_swap_b32 v109, v117
	v_lshl_add_u32 v118, v8, 4, v9
	s_waitcnt lgkmcnt(0)
	v_add_u32_e32 v109, v109, v117
	v_permlane32_swap_b32 v110, v118
	v_readlane_b32 s50, v92, 12
	s_lshl_b64 s[16:17], s[16:17], 9
	s_ashr_i32 s19, s18, 31
	s_waitcnt lgkmcnt(0)
	v_add_u32_e32 v110, v110, v118
	v_permlane16_swap_b32 v87, v107
	v_readlane_b32 s20, v92, 4
	s_add_u32 s66, s28, s62
	s_addc_u32 s67, s29, s63
	global_load_dwordx2 v[24:25], v121, s[66:67]
	s_add_u32 s66, s30, s62
	s_addc_u32 s67, s31, s63
	global_load_dwordx2 v[38:39], v121, s[66:67]
	s_waitcnt lgkmcnt(0)
	v_add_u32_e32 v87, v87, v107
	v_permlane16_swap_b32 v104, v108
	s_lshl_b64 s[38:39], s[38:39], 9
	s_ashr_i32 s51, s50, 31
	v_readlane_b32 s52, v92, 13
	s_waitcnt lgkmcnt(0)
	v_add_u32_e32 v104, v104, v108
	v_permlane16_swap_b32 v105, v109
	s_lshl_b64 s[18:19], s[18:19], 9
	s_ashr_i32 s21, s20, 31
	v_readlane_b32 s22, v92, 5
	s_waitcnt lgkmcnt(0)
	v_add_u32_e32 v105, v105, v109
	v_permlane16_swap_b32 v106, v110
	s_add_u32 s66, s34, s62
	s_addc_u32 s67, s35, s63
	global_load_dwordx2 v[50:51], v121, s[66:67]
	s_lshl_b64 s[50:51], s[50:51], 9
	s_ashr_i32 s53, s52, 31
	s_waitcnt lgkmcnt(0)
	v_add_u32_e32 v106, v106, v110
	v_cndmask_b32_e64 v107, v87, v105, s[44:45]
	v_cndmask_b32_e64 v87, v105, v87, s[44:45]
	s_nop 0
	v_readlane_b32 s54, v92, 14
	s_lshl_b64 s[20:21], s[20:21], 9
	s_ashr_i32 s23, s22, 31
	v_readlane_b32 s24, v92, 6
	s_waitcnt lgkmcnt(0)
	v_add_u32_dpp v87, v107, v87 row_ror:8 row_mask:0xf bank_mask:0xf
	v_cndmask_b32_e64 v105, v104, v106, s[44:45]
	s_nop 1
	v_cndmask_b32_e64 v104, v106, v104, s[44:45]
	s_lshl_b64 s[52:53], s[52:53], 9
	s_ashr_i32 s55, s54, 31
	v_readlane_b32 s56, v92, 15
	s_waitcnt lgkmcnt(0)
	v_add_u32_dpp v104, v105, v104 row_ror:8 row_mask:0xf bank_mask:0xf
	v_cndmask_b32_e64 v105, v87, v104, s[46:47]
	v_cndmask_b32_e64 v87, v104, v87, s[46:47]
	s_nop 0
	v_mov_b32_dpp v104, v105 row_half_mirror row_mask:0xf bank_mask:0xf
	s_nop 1
	s_lshl_b64 s[22:23], s[22:23], 9
	s_ashr_i32 s25, s24, 31
	v_readlane_b32 s26, v92, 7
	s_lshl_b64 s[54:55], s[54:55], 9
	s_waitcnt lgkmcnt(0)
	v_add_u32_dpp v87, v104, v87 quad_perm:[3,2,1,0] row_mask:0xf bank_mask:0xf
	s_nop 1
	s_ashr_i32 s57, s56, 31
	s_lshl_b64 s[24:25], s[24:25], 9
	s_ashr_i32 s27, s26, 31
	s_lshl_b64 s[56:57], s[56:57], 9
	s_waitcnt lgkmcnt(0)
	v_add_u32_dpp v87, v87, v87 quad_perm:[2,3,0,1] row_mask:0xf bank_mask:0xf
	s_nop 1
	s_lshl_b64 s[26:27], s[26:27], 9
	s_waitcnt lgkmcnt(0)
	v_add_u32_dpp v87, v87, v87 quad_perm:[1,0,3,2] row_mask:0xf bank_mask:0xf
	v_cvt_f32_i32_e32 v87, v87
	v_add_f32_e32 v87, v95, v87
	v_mul_f32_e32 v85, v85, v87
	v_mul_f32_e32 v87, 0x3d372713, v85
	v_mul_f32_e32 v87, v85, v87
	v_fma_f32 v87, v85, v87, v85
	v_mul_f32_e32 v87, 0x3fcc422a, v87
	v_mul_f32_e32 v87, 0xbfb8aa3b, v87
	v_exp_f32_e32 v87, v87
	v_lshlrev_b32_e32 v104, 4, v82
	v_add_f32_e32 v87, 1.0, v87
	v_rcp_f32_e32 v87, v87
	s_nop 0
	v_pk_mul_f32 v[84:85], v[84:85], v[86:87]
	v_lshrrev_b32_e32 v87, 4, v82
	v_pk_mul_f32 v[84:85], v[84:85], v[84:85] op_sel:[0,1] op_sel_hi:[1,0]
	v_cvt_f16_f32_e32 v120, v84
	v_and_b32_e32 v86, 0x7070707, v82
	v_readlane_b32 s36, v120, 0
	v_and_b32_e32 v87, 0x7070707, v87
	v_perm_b32 v86, s2, v205, v86
	v_perm_b32 v87, s2, v205, v87
	v_and_or_b32 v86, v104, s4, v86
	v_and_or_b32 v82, v82, s4, v87
	v_perm_b32 v87, v82, v86, s5
	v_perm_b32 v104, v82, v86, s33
	v_perm_b32 v105, v82, v86, s0
	v_perm_b32 v82, v82, v86, s1
	v_pk_fma_f16 v86, v87, s36, v103 op_sel_hi:[1,0,1]
	v_pk_fma_f16 v87, v104, s36, v102 op_sel_hi:[1,0,1]
	v_lshrrev_b32_e32 v102, 4, v83
	v_pk_fma_f16 v82, v82, s36, v100 op_sel_hi:[1,0,1]
	v_and_b32_e32 v100, 0x7070707, v83
	v_and_b32_e32 v102, 0x7070707, v102
	v_perm_b32 v100, s2, v205, v100
	v_perm_b32 v102, s2, v205, v102
	v_lshlrev_b32_e32 v103, 4, v83
	v_and_or_b32 v100, v103, s4, v100
	v_and_or_b32 v83, v83, s4, v102
	v_perm_b32 v102, v83, v100, s5
	v_perm_b32 v103, v83, v100, s33
	v_perm_b32 v104, v83, v100, s0
	v_perm_b32 v83, v83, v100, s1
	v_readlane_b32 s59, v120, 4
	v_lshrrev_b32_e32 v100, 4, v80
	v_pk_fma_f16 v101, v105, s36, v101 op_sel_hi:[1,0,1]
	v_pk_fma_f16 v99, v102, s36, v99 op_sel_hi:[1,0,1]
	v_pk_fma_f16 v98, v103, s36, v98 op_sel_hi:[1,0,1]
	v_pk_fma_f16 v97, v104, s36, v97 op_sel_hi:[1,0,1]
	v_pk_fma_f16 v83, v83, s36, v96 op_sel_hi:[1,0,1]
	v_and_b32_e32 v96, 0x7070707, v80
	v_and_b32_e32 v100, 0x7070707, v100
	v_perm_b32 v96, s2, v205, v96
	v_perm_b32 v100, s2, v205, v100
	v_lshlrev_b32_e32 v102, 4, v80
	v_and_or_b32 v96, v102, s4, v96
	v_and_or_b32 v80, v80, s4, v100
	v_perm_b32 v100, v80, v96, s5
	v_perm_b32 v102, v80, v96, s33
	v_perm_b32 v103, v80, v96, s0
	v_perm_b32 v80, v80, v96, s1
	v_pk_fma_f16 v86, v100, s59, v86 op_sel_hi:[1,0,1]
	v_lshrrev_b32_e32 v100, 4, v81
	v_pk_fma_f16 v80, v80, s59, v82 op_sel_hi:[1,0,1]
	v_and_b32_e32 v82, 0x7070707, v81
	v_and_b32_e32 v100, 0x7070707, v100
	v_pk_fma_f16 v96, v103, s59, v101 op_sel_hi:[1,0,1]
	v_perm_b32 v82, s2, v205, v82
	v_perm_b32 v100, s2, v205, v100
	v_lshlrev_b32_e32 v101, 4, v81
	v_and_or_b32 v82, v101, s4, v82
	v_and_or_b32 v81, v81, s4, v100
	v_perm_b32 v100, v81, v82, s5
	v_pk_fma_f16 v87, v102, s59, v87 op_sel_hi:[1,0,1]
	v_perm_b32 v101, v81, v82, s33
	v_perm_b32 v102, v81, v82, s0
	v_perm_b32 v81, v81, v82, s1
	v_pk_fma_f16 v82, v100, s59, v99 op_sel_hi:[1,0,1]
	v_readlane_b32 s60, v120, 8
	v_lshrrev_b32_e32 v99, 4, v78
	v_pk_fma_f16 v98, v101, s59, v98 op_sel_hi:[1,0,1]
	v_pk_fma_f16 v97, v102, s59, v97 op_sel_hi:[1,0,1]
	v_pk_fma_f16 v81, v81, s59, v83 op_sel_hi:[1,0,1]
	v_and_b32_e32 v85, 0x7070707, v78
	v_and_b32_e32 v99, 0x7070707, v99
	v_perm_b32 v85, s2, v205, v85
	v_perm_b32 v99, s2, v205, v99
	v_lshlrev_b32_e32 v100, 4, v78
	v_and_or_b32 v85, v100, s4, v85
	v_and_or_b32 v78, v78, s4, v99
	v_perm_b32 v99, v78, v85, s5
	v_perm_b32 v100, v78, v85, s33
	v_perm_b32 v101, v78, v85, s0
	v_perm_b32 v78, v78, v85, s1
	v_pk_fma_f16 v85, v99, s60, v86 op_sel_hi:[1,0,1]
	v_pk_fma_f16 v86, v100, s60, v87 op_sel_hi:[1,0,1]
	v_pk_fma_f16 v87, v101, s60, v96 op_sel_hi:[1,0,1]
	v_lshrrev_b32_e32 v96, 4, v79
	v_pk_fma_f16 v78, v78, s60, v80 op_sel_hi:[1,0,1]
	v_and_b32_e32 v80, 0x7070707, v79
	v_and_b32_e32 v96, 0x7070707, v96
	v_perm_b32 v80, s2, v205, v80
	v_perm_b32 v96, s2, v205, v96
	v_lshlrev_b32_e32 v99, 4, v79
	v_and_or_b32 v80, v99, s4, v80
	v_and_or_b32 v79, v79, s4, v96
	v_perm_b32 v96, v79, v80, s5
	v_perm_b32 v100, v79, v80, s0
	v_perm_b32 v99, v79, v80, s33
	v_perm_b32 v79, v79, v80, s1
	v_pk_fma_f16 v80, v96, s60, v82 op_sel_hi:[1,0,1]
	v_pk_fma_f16 v96, v100, s60, v97 op_sel_hi:[1,0,1]
	v_readlane_b32 s36, v120, 12
	v_lshrrev_b32_e32 v97, 4, v76
	v_pk_fma_f16 v82, v99, s60, v98 op_sel_hi:[1,0,1]
	v_pk_fma_f16 v79, v79, s60, v81 op_sel_hi:[1,0,1]
	v_and_b32_e32 v83, 0x7070707, v76
	v_and_b32_e32 v97, 0x7070707, v97
	v_perm_b32 v83, s2, v205, v83
	v_perm_b32 v97, s2, v205, v97
	v_lshlrev_b32_e32 v98, 4, v76
	v_and_or_b32 v83, v98, s4, v83
	v_and_or_b32 v76, v76, s4, v97
	v_perm_b32 v97, v76, v83, s5
	v_perm_b32 v98, v76, v83, s33
	v_perm_b32 v99, v76, v83, s0
	v_perm_b32 v76, v76, v83, s1
	v_pk_fma_f16 v83, v97, s36, v85 op_sel_hi:[1,0,1]
	v_pk_fma_f16 v85, v98, s36, v86 op_sel_hi:[1,0,1]
	v_pk_fma_f16 v86, v99, s36, v87 op_sel_hi:[1,0,1]
	v_lshrrev_b32_e32 v87, 4, v77
	v_pk_fma_f16 v76, v76, s36, v78 op_sel_hi:[1,0,1]
	v_and_b32_e32 v78, 0x7070707, v77
	v_and_b32_e32 v87, 0x7070707, v87
	v_perm_b32 v78, s2, v205, v78
	v_perm_b32 v87, s2, v205, v87
	v_lshlrev_b32_e32 v97, 4, v77
	v_and_or_b32 v78, v97, s4, v78
	v_and_or_b32 v77, v77, s4, v87
	v_perm_b32 v87, v77, v78, s5
	v_perm_b32 v97, v77, v78, s33
	v_perm_b32 v98, v77, v78, s0
	v_perm_b32 v77, v77, v78, s1
	v_pk_fma_f16 v78, v87, s36, v80 op_sel_hi:[1,0,1]
	v_readlane_b32 s59, v120, 16
	v_lshrrev_b32_e32 v87, 4, v74
	v_pk_fma_f16 v80, v97, s36, v82 op_sel_hi:[1,0,1]
	v_pk_fma_f16 v82, v98, s36, v96 op_sel_hi:[1,0,1]
	v_pk_fma_f16 v77, v77, s36, v79 op_sel_hi:[1,0,1]
	v_and_b32_e32 v81, 0x7070707, v74
	v_and_b32_e32 v87, 0x7070707, v87
	v_perm_b32 v81, s2, v205, v81
	v_perm_b32 v87, s2, v205, v87
	v_lshlrev_b32_e32 v96, 4, v74
	v_and_or_b32 v81, v96, s4, v81
	v_and_or_b32 v74, v74, s4, v87
	v_perm_b32 v87, v74, v81, s5
	v_perm_b32 v96, v74, v81, s33
	v_perm_b32 v97, v74, v81, s0
	v_perm_b32 v74, v74, v81, s1
	v_pk_fma_f16 v81, v87, s59, v83 op_sel_hi:[1,0,1]
	v_pk_fma_f16 v83, v96, s59, v85 op_sel_hi:[1,0,1]
	v_pk_fma_f16 v85, v97, s59, v86 op_sel_hi:[1,0,1]
	v_lshrrev_b32_e32 v86, 4, v75
	v_pk_fma_f16 v74, v74, s59, v76 op_sel_hi:[1,0,1]
	v_and_b32_e32 v76, 0x7070707, v75
	v_and_b32_e32 v86, 0x7070707, v86
	v_perm_b32 v76, s2, v205, v76
	v_perm_b32 v86, s2, v205, v86
	v_lshlrev_b32_e32 v87, 4, v75
	v_and_or_b32 v76, v87, s4, v76
	v_and_or_b32 v75, v75, s4, v86
	v_perm_b32 v86, v75, v76, s5
	v_perm_b32 v87, v75, v76, s33
	v_perm_b32 v96, v75, v76, s0
	v_perm_b32 v75, v75, v76, s1
	v_pk_fma_f16 v76, v86, s59, v78 op_sel_hi:[1,0,1]
	v_pk_fma_f16 v78, v87, s59, v80 op_sel_hi:[1,0,1]
	v_pk_fma_f16 v80, v96, s59, v82 op_sel_hi:[1,0,1]
	v_readlane_b32 s60, v120, 20
	v_lshrrev_b32_e32 v82, 4, v70
	v_pk_fma_f16 v75, v75, s59, v77 op_sel_hi:[1,0,1]
	v_and_b32_e32 v79, 0x7070707, v70
	v_and_b32_e32 v82, 0x7070707, v82
	v_perm_b32 v79, s2, v205, v79
	v_perm_b32 v82, s2, v205, v82
	v_lshlrev_b32_e32 v86, 4, v70
	v_and_or_b32 v79, v86, s4, v79
	v_and_or_b32 v70, v70, s4, v82
	v_perm_b32 v82, v70, v79, s5
	v_perm_b32 v86, v70, v79, s33
	v_perm_b32 v87, v70, v79, s0
	v_perm_b32 v70, v70, v79, s1
	v_pk_fma_f16 v79, v82, s60, v81 op_sel_hi:[1,0,1]
	v_pk_fma_f16 v81, v86, s60, v83 op_sel_hi:[1,0,1]
	v_lshrrev_b32_e32 v83, 4, v71
	v_pk_fma_f16 v70, v70, s60, v74 op_sel_hi:[1,0,1]
	v_and_b32_e32 v74, 0x7070707, v71
	v_and_b32_e32 v83, 0x7070707, v83
	v_pk_fma_f16 v82, v87, s60, v85 op_sel_hi:[1,0,1]
	v_perm_b32 v74, s2, v205, v74
	v_perm_b32 v83, s2, v205, v83
	v_lshlrev_b32_e32 v85, 4, v71
	v_and_or_b32 v74, v85, s4, v74
	v_and_or_b32 v71, v71, s4, v83
	v_perm_b32 v83, v71, v74, s5
	v_perm_b32 v85, v71, v74, s33
	v_perm_b32 v86, v71, v74, s0
	v_perm_b32 v71, v71, v74, s1
	v_pk_fma_f16 v74, v83, s60, v76 op_sel_hi:[1,0,1]
	v_pk_fma_f16 v76, v85, s60, v78 op_sel_hi:[1,0,1]
	v_pk_fma_f16 v78, v86, s60, v80 op_sel_hi:[1,0,1]
	v_readlane_b32 s36, v120, 24
	v_lshrrev_b32_e32 v80, 4, v68
	v_pk_fma_f16 v71, v71, s60, v75 op_sel_hi:[1,0,1]
	v_and_b32_e32 v77, 0x7070707, v68
	v_and_b32_e32 v80, 0x7070707, v80
	v_perm_b32 v77, s2, v205, v77
	v_perm_b32 v80, s2, v205, v80
	v_lshlrev_b32_e32 v83, 4, v68
	v_and_or_b32 v77, v83, s4, v77
	v_and_or_b32 v68, v68, s4, v80
	v_perm_b32 v80, v68, v77, s5
	v_perm_b32 v83, v68, v77, s33
	v_perm_b32 v85, v68, v77, s0
	v_perm_b32 v68, v68, v77, s1
	v_pk_fma_f16 v77, v80, s36, v79 op_sel_hi:[1,0,1]
	v_pk_fma_f16 v79, v83, s36, v81 op_sel_hi:[1,0,1]
	v_lshrrev_b32_e32 v81, 4, v69
	v_pk_fma_f16 v68, v68, s36, v70 op_sel_hi:[1,0,1]
	v_and_b32_e32 v70, 0x7070707, v69
	v_and_b32_e32 v81, 0x7070707, v81
	v_pk_fma_f16 v80, v85, s36, v82 op_sel_hi:[1,0,1]
	v_perm_b32 v70, s2, v205, v70
	v_perm_b32 v81, s2, v205, v81
	v_lshlrev_b32_e32 v82, 4, v69
	v_and_or_b32 v70, v82, s4, v70
	v_and_or_b32 v69, v69, s4, v81
	v_perm_b32 v81, v69, v70, s5
	v_perm_b32 v82, v69, v70, s33
	v_perm_b32 v83, v69, v70, s0
	v_perm_b32 v69, v69, v70, s1
	v_pk_fma_f16 v70, v81, s36, v74 op_sel_hi:[1,0,1]
	v_pk_fma_f16 v74, v82, s36, v76 op_sel_hi:[1,0,1]
	v_pk_fma_f16 v76, v83, s36, v78 op_sel_hi:[1,0,1]
	v_readlane_b32 s59, v120, 28
	v_lshrrev_b32_e32 v78, 4, v64
	v_pk_fma_f16 v69, v69, s36, v71 op_sel_hi:[1,0,1]
	v_and_b32_e32 v75, 0x7070707, v64
	v_and_b32_e32 v78, 0x7070707, v78
	v_perm_b32 v75, s2, v205, v75
	v_perm_b32 v78, s2, v205, v78
	v_lshlrev_b32_e32 v81, 4, v64
	v_and_or_b32 v75, v81, s4, v75
	v_and_or_b32 v64, v64, s4, v78
	v_perm_b32 v78, v64, v75, s5
	v_perm_b32 v81, v64, v75, s33
	v_perm_b32 v82, v64, v75, s0
	v_perm_b32 v64, v64, v75, s1
	v_pk_fma_f16 v75, v78, s59, v77 op_sel_hi:[1,0,1]
	v_pk_fma_f16 v77, v81, s59, v79 op_sel_hi:[1,0,1]
	v_lshrrev_b32_e32 v79, 4, v65
	v_pk_fma_f16 v64, v64, s59, v68 op_sel_hi:[1,0,1]
	v_and_b32_e32 v68, 0x7070707, v65
	v_and_b32_e32 v79, 0x7070707, v79
	v_pk_fma_f16 v78, v82, s59, v80 op_sel_hi:[1,0,1]
	v_perm_b32 v68, s2, v205, v68
	v_perm_b32 v79, s2, v205, v79
	v_lshlrev_b32_e32 v80, 4, v65
	v_and_or_b32 v68, v80, s4, v68
	v_and_or_b32 v65, v65, s4, v79
	v_perm_b32 v79, v65, v68, s5
	v_perm_b32 v80, v65, v68, s33
	v_perm_b32 v81, v65, v68, s0
	v_perm_b32 v65, v65, v68, s1
	v_pk_fma_f16 v68, v79, s59, v70 op_sel_hi:[1,0,1]
	v_pk_fma_f16 v70, v80, s59, v74 op_sel_hi:[1,0,1]
	v_pk_fma_f16 v74, v81, s59, v76 op_sel_hi:[1,0,1]
	v_readlane_b32 s60, v120, 32
	v_lshrrev_b32_e32 v76, 4, v62
	v_pk_fma_f16 v65, v65, s59, v69 op_sel_hi:[1,0,1]
	v_and_b32_e32 v71, 0x7070707, v62
	v_and_b32_e32 v76, 0x7070707, v76
	v_perm_b32 v71, s2, v205, v71
	v_perm_b32 v76, s2, v205, v76
	v_lshlrev_b32_e32 v79, 4, v62
	v_and_or_b32 v71, v79, s4, v71
	v_and_or_b32 v62, v62, s4, v76
	v_perm_b32 v76, v62, v71, s5
	v_perm_b32 v79, v62, v71, s33
	v_perm_b32 v80, v62, v71, s0
	v_perm_b32 v62, v62, v71, s1
	v_pk_fma_f16 v71, v76, s60, v75 op_sel_hi:[1,0,1]
	v_pk_fma_f16 v75, v79, s60, v77 op_sel_hi:[1,0,1]
	v_lshrrev_b32_e32 v77, 4, v63
	v_pk_fma_f16 v62, v62, s60, v64 op_sel_hi:[1,0,1]
	v_and_b32_e32 v64, 0x7070707, v63
	v_and_b32_e32 v77, 0x7070707, v77
	v_pk_fma_f16 v76, v80, s60, v78 op_sel_hi:[1,0,1]
	v_perm_b32 v64, s2, v205, v64
	v_perm_b32 v77, s2, v205, v77
	v_lshlrev_b32_e32 v78, 4, v63
	v_and_or_b32 v64, v78, s4, v64
	v_and_or_b32 v63, v63, s4, v77
	v_perm_b32 v77, v63, v64, s5
	v_perm_b32 v78, v63, v64, s33
	v_perm_b32 v79, v63, v64, s0
	v_perm_b32 v63, v63, v64, s1
	v_pk_fma_f16 v64, v77, s60, v68 op_sel_hi:[1,0,1]
	v_pk_fma_f16 v68, v78, s60, v70 op_sel_hi:[1,0,1]
	v_pk_fma_f16 v70, v79, s60, v74 op_sel_hi:[1,0,1]
	v_readlane_b32 s36, v120, 36
	v_lshrrev_b32_e32 v74, 4, v66
	v_pk_fma_f16 v63, v63, s60, v65 op_sel_hi:[1,0,1]
	v_and_b32_e32 v69, 0x7070707, v66
	v_and_b32_e32 v74, 0x7070707, v74
	v_perm_b32 v69, s2, v205, v69
	v_perm_b32 v74, s2, v205, v74
	v_lshlrev_b32_e32 v77, 4, v66
	v_and_or_b32 v69, v77, s4, v69
	v_and_or_b32 v66, v66, s4, v74
	v_perm_b32 v74, v66, v69, s5
	v_perm_b32 v77, v66, v69, s33
	v_perm_b32 v78, v66, v69, s0
	v_perm_b32 v66, v66, v69, s1
	v_pk_fma_f16 v69, v74, s36, v71 op_sel_hi:[1,0,1]
	v_pk_fma_f16 v71, v77, s36, v75 op_sel_hi:[1,0,1]
	v_lshrrev_b32_e32 v75, 4, v67
	v_pk_fma_f16 v62, v66, s36, v62 op_sel_hi:[1,0,1]
	v_and_b32_e32 v66, 0x7070707, v67
	v_and_b32_e32 v75, 0x7070707, v75
	v_pk_fma_f16 v74, v78, s36, v76 op_sel_hi:[1,0,1]
	v_perm_b32 v66, s2, v205, v66
	v_perm_b32 v75, s2, v205, v75
	v_lshlrev_b32_e32 v76, 4, v67
	v_and_or_b32 v66, v76, s4, v66
	v_and_or_b32 v67, v67, s4, v75
	v_perm_b32 v76, v67, v66, s33
	v_perm_b32 v77, v67, v66, s0
	v_perm_b32 v75, v67, v66, s5
	v_perm_b32 v66, v67, v66, s1
	v_pk_fma_f16 v67, v76, s36, v68 op_sel_hi:[1,0,1]
	v_pk_fma_f16 v68, v77, s36, v70 op_sel_hi:[1,0,1]
	v_readlane_b32 s59, v120, 40
	v_lshrrev_b32_e32 v70, 4, v60
	v_pk_fma_f16 v64, v75, s36, v64 op_sel_hi:[1,0,1]
	v_pk_fma_f16 v63, v66, s36, v63 op_sel_hi:[1,0,1]
	v_and_b32_e32 v66, 0x7070707, v60
	v_and_b32_e32 v70, 0x7070707, v70
	v_perm_b32 v66, s2, v205, v66
	v_perm_b32 v70, s2, v205, v70
	v_lshlrev_b32_e32 v75, 4, v60
	v_and_or_b32 v66, v75, s4, v66
	v_and_or_b32 v60, v60, s4, v70
	v_perm_b32 v70, v60, v66, s5
	v_perm_b32 v75, v60, v66, s33
	v_perm_b32 v76, v60, v66, s0
	v_perm_b32 v60, v60, v66, s1
	v_pk_fma_f16 v66, v70, s59, v69 op_sel_hi:[1,0,1]
	v_pk_fma_f16 v69, v75, s59, v71 op_sel_hi:[1,0,1]
	v_lshrrev_b32_e32 v71, 4, v61
	v_pk_fma_f16 v60, v60, s59, v62 op_sel_hi:[1,0,1]
	v_and_b32_e32 v62, 0x7070707, v61
	v_and_b32_e32 v71, 0x7070707, v71
	v_pk_fma_f16 v70, v76, s59, v74 op_sel_hi:[1,0,1]
	v_perm_b32 v62, s2, v205, v62
	v_perm_b32 v71, s2, v205, v71
	v_lshlrev_b32_e32 v74, 4, v61
	v_and_or_b32 v62, v74, s4, v62
	v_and_or_b32 v61, v61, s4, v71
	v_perm_b32 v71, v61, v62, s5
	v_perm_b32 v74, v61, v62, s33
	v_perm_b32 v75, v61, v62, s0
	v_perm_b32 v61, v61, v62, s1
	v_pk_fma_f16 v62, v71, s59, v64 op_sel_hi:[1,0,1]
	v_pk_fma_f16 v64, v74, s59, v67 op_sel_hi:[1,0,1]
	v_pk_fma_f16 v67, v75, s59, v68 op_sel_hi:[1,0,1]
	v_readlane_b32 s60, v120, 44
	v_lshrrev_b32_e32 v68, 4, v58
	v_pk_fma_f16 v61, v61, s59, v63 op_sel_hi:[1,0,1]
	v_and_b32_e32 v65, 0x7070707, v58
	v_and_b32_e32 v68, 0x7070707, v68
	v_perm_b32 v65, s2, v205, v65
	v_perm_b32 v68, s2, v205, v68
	v_lshlrev_b32_e32 v71, 4, v58
	v_and_or_b32 v65, v71, s4, v65
	v_and_or_b32 v58, v58, s4, v68
	v_perm_b32 v68, v58, v65, s5
	v_perm_b32 v71, v58, v65, s33
	v_perm_b32 v74, v58, v65, s0
	v_perm_b32 v58, v58, v65, s1
	v_pk_fma_f16 v65, v68, s60, v66 op_sel_hi:[1,0,1]
	v_pk_fma_f16 v66, v71, s60, v69 op_sel_hi:[1,0,1]
	v_lshrrev_b32_e32 v69, 4, v59
	v_pk_fma_f16 v58, v58, s60, v60 op_sel_hi:[1,0,1]
	v_and_b32_e32 v60, 0x7070707, v59
	v_and_b32_e32 v69, 0x7070707, v69
	v_pk_fma_f16 v68, v74, s60, v70 op_sel_hi:[1,0,1]
	v_perm_b32 v60, s2, v205, v60
	v_perm_b32 v69, s2, v205, v69
	v_lshlrev_b32_e32 v70, 4, v59
	v_and_or_b32 v60, v70, s4, v60
	v_and_or_b32 v59, v59, s4, v69
	v_perm_b32 v69, v59, v60, s5
	v_perm_b32 v70, v59, v60, s33
	v_perm_b32 v71, v59, v60, s0
	v_perm_b32 v59, v59, v60, s1
	v_pk_fma_f16 v60, v69, s60, v62 op_sel_hi:[1,0,1]
	v_pk_fma_f16 v62, v70, s60, v64 op_sel_hi:[1,0,1]
	v_pk_fma_f16 v64, v71, s60, v67 op_sel_hi:[1,0,1]
	v_readlane_b32 s36, v120, 48
	v_lshrrev_b32_e32 v67, 4, v56
	v_pk_fma_f16 v59, v59, s60, v61 op_sel_hi:[1,0,1]
	v_and_b32_e32 v63, 0x7070707, v56
	v_and_b32_e32 v67, 0x7070707, v67
	v_perm_b32 v63, s2, v205, v63
	v_perm_b32 v67, s2, v205, v67
	v_lshlrev_b32_e32 v69, 4, v56
	v_and_or_b32 v63, v69, s4, v63
	v_and_or_b32 v56, v56, s4, v67
	v_perm_b32 v67, v56, v63, s5
	v_perm_b32 v69, v56, v63, s33
	v_perm_b32 v70, v56, v63, s0
	v_perm_b32 v56, v56, v63, s1
	v_pk_fma_f16 v63, v67, s36, v65 op_sel_hi:[1,0,1]
	v_lshrrev_b32_e32 v67, 4, v57
	v_pk_fma_f16 v56, v56, s36, v58 op_sel_hi:[1,0,1]
	v_and_b32_e32 v58, 0x7070707, v57
	v_and_b32_e32 v67, 0x7070707, v67
	v_pk_fma_f16 v65, v69, s36, v66 op_sel_hi:[1,0,1]
	v_pk_fma_f16 v66, v70, s36, v68 op_sel_hi:[1,0,1]
	v_perm_b32 v58, s2, v205, v58
	v_perm_b32 v67, s2, v205, v67
	v_lshlrev_b32_e32 v68, 4, v57
	v_and_or_b32 v58, v68, s4, v58
	v_and_or_b32 v57, v57, s4, v67
	v_perm_b32 v67, v57, v58, s5
	v_perm_b32 v68, v57, v58, s33
	v_perm_b32 v69, v57, v58, s0
	v_perm_b32 v57, v57, v58, s1
	v_pk_fma_f16 v58, v67, s36, v60 op_sel_hi:[1,0,1]
	v_pk_fma_f16 v60, v68, s36, v62 op_sel_hi:[1,0,1]
	v_pk_fma_f16 v62, v69, s36, v64 op_sel_hi:[1,0,1]
	v_readlane_b32 s59, v120, 52
	v_lshrrev_b32_e32 v64, 4, v54
	v_pk_fma_f16 v57, v57, s36, v59 op_sel_hi:[1,0,1]
	v_and_b32_e32 v61, 0x7070707, v54
	v_and_b32_e32 v64, 0x7070707, v64
	v_perm_b32 v61, s2, v205, v61
	v_perm_b32 v64, s2, v205, v64
	v_lshlrev_b32_e32 v67, 4, v54
	v_and_or_b32 v61, v67, s4, v61
	v_and_or_b32 v54, v54, s4, v64
	v_perm_b32 v64, v54, v61, s5
	v_perm_b32 v67, v54, v61, s33
	v_perm_b32 v68, v54, v61, s0
	v_perm_b32 v54, v54, v61, s1
	v_pk_fma_f16 v61, v64, s59, v63 op_sel_hi:[1,0,1]
	v_pk_fma_f16 v63, v67, s59, v65 op_sel_hi:[1,0,1]
	v_lshrrev_b32_e32 v65, 4, v55
	v_pk_fma_f16 v54, v54, s59, v56 op_sel_hi:[1,0,1]
	v_and_b32_e32 v56, 0x7070707, v55
	v_and_b32_e32 v65, 0x7070707, v65
	v_pk_fma_f16 v64, v68, s59, v66 op_sel_hi:[1,0,1]
	v_perm_b32 v56, s2, v205, v56
	v_perm_b32 v65, s2, v205, v65
	v_lshlrev_b32_e32 v66, 4, v55
	v_and_or_b32 v56, v66, s4, v56
	v_and_or_b32 v55, v55, s4, v65
	v_perm_b32 v65, v55, v56, s5
	v_perm_b32 v66, v55, v56, s33
	v_perm_b32 v67, v55, v56, s0
	v_perm_b32 v55, v55, v56, s1
	v_pk_fma_f16 v56, v65, s59, v58 op_sel_hi:[1,0,1]
	v_pk_fma_f16 v58, v66, s59, v60 op_sel_hi:[1,0,1]
	v_pk_fma_f16 v60, v67, s59, v62 op_sel_hi:[1,0,1]
	v_readlane_b32 s60, v120, 56
	v_lshrrev_b32_e32 v62, 4, v52
	v_pk_fma_f16 v55, v55, s59, v57 op_sel_hi:[1,0,1]
	v_and_b32_e32 v59, 0x7070707, v52
	v_and_b32_e32 v62, 0x7070707, v62
	v_perm_b32 v59, s2, v205, v59
	v_perm_b32 v62, s2, v205, v62
	v_lshlrev_b32_e32 v65, 4, v52
	v_and_or_b32 v59, v65, s4, v59
	v_and_or_b32 v52, v52, s4, v62
	v_perm_b32 v62, v52, v59, s5
	v_perm_b32 v65, v52, v59, s33
	v_perm_b32 v66, v52, v59, s0
	v_perm_b32 v52, v52, v59, s1
	v_pk_fma_f16 v59, v62, s60, v61 op_sel_hi:[1,0,1]
	v_pk_fma_f16 v61, v65, s60, v63 op_sel_hi:[1,0,1]
	v_lshrrev_b32_e32 v63, 4, v53
	v_pk_fma_f16 v52, v52, s60, v54 op_sel_hi:[1,0,1]
	v_and_b32_e32 v54, 0x7070707, v53
	v_and_b32_e32 v63, 0x7070707, v63
	v_pk_fma_f16 v62, v66, s60, v64 op_sel_hi:[1,0,1]
	v_perm_b32 v54, s2, v205, v54
	v_perm_b32 v63, s2, v205, v63
	v_lshlrev_b32_e32 v64, 4, v53
	v_and_or_b32 v54, v64, s4, v54
	v_and_or_b32 v53, v53, s4, v63
	v_perm_b32 v63, v53, v54, s5
	v_perm_b32 v64, v53, v54, s33
	v_perm_b32 v65, v53, v54, s0
	v_perm_b32 v53, v53, v54, s1
	v_pk_fma_f16 v54, v63, s60, v56 op_sel_hi:[1,0,1]
	v_pk_fma_f16 v56, v64, s60, v58 op_sel_hi:[1,0,1]
	v_pk_fma_f16 v58, v65, s60, v60 op_sel_hi:[1,0,1]
	v_readlane_b32 s36, v120, 60
	v_lshrrev_b32_e32 v60, 4, v36
	v_pk_fma_f16 v53, v53, s60, v55 op_sel_hi:[1,0,1]
	v_and_b32_e32 v57, 0x7070707, v36
	v_and_b32_e32 v60, 0x7070707, v60
	v_perm_b32 v57, s2, v205, v57
	v_perm_b32 v60, s2, v205, v60
	v_lshlrev_b32_e32 v63, 4, v36
	v_and_or_b32 v57, v63, s4, v57
	v_and_or_b32 v36, v36, s4, v60
	v_perm_b32 v60, v36, v57, s5
	v_perm_b32 v63, v36, v57, s33
	v_perm_b32 v64, v36, v57, s0
	v_perm_b32 v36, v36, v57, s1
	v_pk_fma_f16 v100, v36, s36, v52 op_sel_hi:[1,0,1]
	v_lshrrev_b32_e32 v52, 4, v37
	v_and_b32_e32 v36, 0x7070707, v37
	v_and_b32_e32 v52, 0x7070707, v52
	v_perm_b32 v36, s2, v205, v36
	v_perm_b32 v52, s2, v205, v52
	v_lshlrev_b32_e32 v57, 4, v37
	v_and_or_b32 v36, v57, s4, v36
	v_and_or_b32 v37, v37, s4, v52
	v_pk_fma_f16 v103, v60, s36, v59 op_sel_hi:[1,0,1]
	v_perm_b32 v52, v37, v36, s5
	v_perm_b32 v57, v37, v36, s33
	v_perm_b32 v59, v37, v36, s0
	v_perm_b32 v36, v37, v36, s1
	v_pk_fma_f16 v96, v36, s36, v53 op_sel_hi:[1,0,1]
	s_add_u32 s66, s12, s64
	s_addc_u32 s67, s13, s65
	global_load_dwordx2 v[82:83], v121, s[66:67]
	s_add_u32 s66, s14, s64
	s_addc_u32 s67, s15, s65
	global_load_dwordx2 v[80:81], v121, s[66:67]
	s_add_u32 s66, s38, s62
	s_addc_u32 s67, s39, s63
	global_load_dwordx2 v[48:49], v121, s[66:67]
	s_add_u32 s66, s16, s64
	s_addc_u32 s67, s17, s65
	global_load_dwordx2 v[78:79], v121, s[66:67]
	s_add_u32 s66, s50, s62
	s_addc_u32 s67, s51, s63
	global_load_dwordx2 v[46:47], v121, s[66:67]
	s_add_u32 s66, s18, s64
	s_addc_u32 s67, s19, s65
	global_load_dwordx2 v[76:77], v121, s[66:67]
	s_add_u32 s66, s52, s62
	s_addc_u32 s67, s53, s63
	global_load_dwordx2 v[44:45], v121, s[66:67]
	s_add_u32 s66, s20, s64
	s_addc_u32 s67, s21, s65
	global_load_dwordx2 v[74:75], v121, s[66:67]
	s_add_u32 s66, s54, s62
	s_addc_u32 s67, s55, s63
	global_load_dwordx2 v[42:43], v121, s[66:67]
	s_add_u32 s66, s22, s64
	s_addc_u32 s67, s23, s65
	global_load_dwordx2 v[70:71], v121, s[66:67]
	s_add_u32 s66, s56, s62
	s_addc_u32 s67, s57, s63
	global_load_dwordx2 v[40:41], v121, s[66:67]
	v_pk_fma_f16 v101, v64, s36, v62 op_sel_hi:[1,0,1]
	s_add_u32 s66, s24, s64
	s_addc_u32 s67, s25, s65
	global_load_dwordx2 v[68:69], v121, s[66:67]
	s_add_u32 s66, s26, s64
	s_addc_u32 s67, s27, s65
	global_load_dwordx2 v[64:65], v121, s[66:67]
	v_pk_fma_f16 v102, v63, s36, v61 op_sel_hi:[1,0,1]
	s_add_u32 s66, s28, s64
	s_addc_u32 s67, s29, s65
	global_load_dwordx2 v[62:63], v121, s[66:67]
	s_add_u32 s66, s30, s64
	s_addc_u32 s67, s31, s65
	global_load_dwordx2 v[66:67], v121, s[66:67]
	s_add_u32 s66, s34, s64
	s_addc_u32 s67, s35, s65
	global_load_dwordx2 v[60:61], v121, s[66:67]
	v_pk_fma_f16 v97, v59, s36, v58 op_sel_hi:[1,0,1]
	s_add_u32 s66, s38, s64
	s_addc_u32 s67, s39, s65
	global_load_dwordx2 v[58:59], v121, s[66:67]
	v_pk_fma_f16 v98, v57, s36, v56 op_sel_hi:[1,0,1]
	s_add_u32 s66, s50, s64
	s_addc_u32 s67, s51, s65
	global_load_dwordx2 v[56:57], v121, s[66:67]
	v_pk_fma_f16 v99, v52, s36, v54 op_sel_hi:[1,0,1]
	s_add_u32 s66, s52, s64
	s_addc_u32 s67, s53, s65
	global_load_dwordx2 v[54:55], v121, s[66:67]
	s_add_u32 s66, s54, s64
	s_addc_u32 s67, s55, s65
	global_load_dwordx2 v[52:53], v121, s[66:67]
	s_add_u32 s66, s12, s62
	s_addc_u32 s67, s13, s63
	global_load_dwordx2 v[8:9], v121, s[66:67]
	s_add_u32 s66, s14, s62
	s_addc_u32 s67, s15, s63
	global_load_dwordx2 v[10:11], v121, s[66:67]
	s_nop 0
	s_add_u32 s66, s16, s62
	s_addc_u32 s67, s17, s63
	global_load_dwordx2 v[12:13], v121, s[66:67]
	s_nop 0
	s_add_u32 s66, s18, s62
	s_addc_u32 s67, s19, s63
	global_load_dwordx2 v[14:15], v121, s[66:67]
	s_nop 0
	s_add_u32 s66, s20, s62
	s_addc_u32 s67, s21, s63
	global_load_dwordx2 v[16:17], v121, s[66:67]
	s_nop 0
	s_add_u32 s66, s22, s62
	s_addc_u32 s67, s23, s63
	global_load_dwordx2 v[18:19], v121, s[66:67]
	s_nop 0
	s_add_u32 s66, s24, s62
	s_addc_u32 s67, s25, s63
	global_load_dwordx2 v[20:21], v121, s[66:67]
	s_nop 0
	s_add_u32 s66, s26, s62
	s_addc_u32 s67, s27, s63
	global_load_dwordx2 v[22:23], v121, s[66:67]
	s_nop 0
	s_add_u32 s66, s56, s64
	s_addc_u32 s67, s57, s65
	global_load_dwordx2 v[36:37], v121, s[66:67]
	s_cmpk_eq_i32 s58, 0x90
	s_cbranch_scc0 .LBB0_763
	v_lshlrev_b64 v[0:1], 2, v[2:3]
	v_lshl_add_u64 v[2:3], v[28:29], 0, v[0:1]
	v_mov_b32_e32 v104, v208
	v_mov_b32_e32 v105, v209
	v_mov_b32_e32 v106, v210
	v_mov_b32_e32 v107, v211
	v_mov_b32_e32 v108, v212
	v_mov_b32_e32 v109, v213
	v_mov_b32_e32 v110, v214
	v_mov_b32_e32 v111, v215
	v_mov_b32_e32 v86, v216
	v_mov_b32_e32 v87, v217
	v_mov_b32_e32 v88, v218
	v_mov_b32_e32 v89, v219
	v_mov_b32_e32 v112, v220
	v_mov_b32_e32 v113, v221
	v_mov_b32_e32 v114, v222
	v_mov_b32_e32 v115, v223
	v_lshl_add_u64 v[72:73], v[32:33], 0, v[0:1]
	v_cvt_f32_f16_sdwa v1, v103 dst_sel:DWORD dst_unused:UNUSED_PAD src0_sel:WORD_1
	v_cvt_f32_f16_e32 v0, v103
	v_cvt_f32_f16_sdwa v91, v102 dst_sel:DWORD dst_unused:UNUSED_PAD src0_sel:WORD_1
	v_cvt_f32_f16_e32 v90, v102
	v_cvt_f32_f16_sdwa v103, v101 dst_sel:DWORD dst_unused:UNUSED_PAD src0_sel:WORD_1
	v_cvt_f32_f16_e32 v102, v101
	v_cvt_f32_f16_sdwa v101, v100 dst_sel:DWORD dst_unused:UNUSED_PAD src0_sel:WORD_1
	v_cvt_f32_f16_e32 v100, v100
	s_mov_b32 s18, 0x800000
	v_readlane_b32 s12, v255, 5
	v_readlane_b32 s13, v255, 6
	v_pk_add_f32 v[86:87], v[86:87], v[102:103]
	v_pk_add_f32 v[84:85], v[112:113], v[0:1]
	v_mov_b32_e32 v102, v85
	v_mov_b32_e32 v103, v87
	v_pk_add_f32 v[90:91], v[114:115], v[90:91]
	v_pk_add_f32 v[88:89], v[88:89], v[100:101]
	v_mov_b32_e32 v100, v84
	v_mov_b32_e32 v101, v86
	v_pk_mul_f32 v[102:103], v[102:103], v[102:103]
	v_mov_b32_e32 v112, v91
	v_pk_fma_f32 v[100:101], v[100:101], v[100:101], v[102:103]
	v_mov_b32_e32 v102, v90
	v_mov_b32_e32 v103, v88
	v_pk_fma_f32 v[100:101], v[102:103], v[102:103], v[100:101]
	v_cvt_f32_f16_sdwa v103, v99 dst_sel:DWORD dst_unused:UNUSED_PAD src0_sel:WORD_1
	v_cvt_f32_f16_e32 v102, v99
	v_cvt_f32_f16_sdwa v99, v98 dst_sel:DWORD dst_unused:UNUSED_PAD src0_sel:WORD_1
	v_cvt_f32_f16_e32 v98, v98
	v_mov_b32_e32 v113, v89
	v_pk_add_f32 v[102:103], v[108:109], v[102:103]
	v_cvt_f32_f16_sdwa v109, v97 dst_sel:DWORD dst_unused:UNUSED_PAD src0_sel:WORD_1
	v_cvt_f32_f16_e32 v108, v97
	v_cvt_f32_f16_sdwa v97, v96 dst_sel:DWORD dst_unused:UNUSED_PAD src0_sel:WORD_1
	v_cvt_f32_f16_e32 v96, v96
	v_pk_add_f32 v[98:99], v[110:111], v[98:99]
	v_pk_add_f32 v[104:105], v[104:105], v[108:109]
	v_mov_b32_e32 v108, v103
	v_mov_b32_e32 v109, v105
	v_pk_add_f32 v[96:97], v[106:107], v[96:97]
	v_mov_b32_e32 v106, v102
	v_mov_b32_e32 v107, v104
	v_pk_mul_f32 v[108:109], v[108:109], v[108:109]
	v_pk_fma_f32 v[100:101], v[112:113], v[112:113], v[100:101]
	v_pk_fma_f32 v[106:107], v[106:107], v[106:107], v[108:109]
	v_mov_b32_e32 v108, v98
	v_mov_b32_e32 v109, v96
	v_mov_b32_e32 v110, v99
	v_mov_b32_e32 v111, v97
	v_pk_fma_f32 v[106:107], v[108:109], v[108:109], v[106:107]
	v_add_f32_e32 v95, v100, v101
	v_pk_fma_f32 v[106:107], v[110:111], v[110:111], v[106:107]
	v_lshl_add_u64 v[34:35], v[34:35], 0, s[12:13]
	v_add_f32_e32 v95, v95, v106
	v_add_f32_e32 v95, v95, v107
	v_mov_b32_e32 v100, v95
	s_nop 1
	v_permlane32_swap_b32 v100, v95
	s_waitcnt lgkmcnt(0)
	v_add_f32_e32 v95, v95, v100
	v_mov_b32_e32 v100, v95
	s_nop 1
	v_permlane16_swap_b32 v100, v95
	s_waitcnt lgkmcnt(0)
	v_add_f32_e32 v95, v95, v100
	s_nop 1
	v_mov_b32_dpp v100, v95 row_ror:8 row_mask:0xf bank_mask:0xf
	s_waitcnt lgkmcnt(0)
	v_add_f32_e32 v95, v95, v100
	s_nop 1
	v_mov_b32_dpp v100, v95 row_half_mirror row_mask:0xf bank_mask:0xf
	s_nop 1
	v_mov_b32_dpp v100, v100 quad_perm:[3,2,1,0] row_mask:0xf bank_mask:0xf
	s_waitcnt lgkmcnt(0)
	v_add_f32_e32 v95, v95, v100
	s_nop 1
	v_mov_b32_dpp v100, v95 quad_perm:[2,3,0,1] row_mask:0xf bank_mask:0xf
	s_waitcnt lgkmcnt(0)
	v_add_f32_e32 v95, v95, v100
	s_nop 1
	v_mov_b32_dpp v100, v95 quad_perm:[1,0,3,2] row_mask:0xf bank_mask:0xf
	s_waitcnt lgkmcnt(0)
	v_add_f32_e32 v95, v95, v100
	v_fmamk_f32 v95, v95, 0x3a800000, v191
	v_cmp_gt_f32_e32 vcc, s18, v95
	v_mul_f32_e32 v100, 0x4b800000, v95
	s_nop 0
	v_cndmask_b32_e32 v95, v95, v100, vcc
	v_rsq_f32_e32 v95, v95
	s_nop 0
	v_mul_f32_e32 v100, 0x45800000, v95
	v_cndmask_b32_e32 v100, v95, v100, vcc
	v_pk_mul_f32 v[84:85], v[84:85], v[100:101] op_sel_hi:[1,0]
	v_pk_mul_f32 v[0:1], v[124:125], v[84:85]
	v_pk_mul_f32 v[84:85], v[90:91], v[100:101] op_sel_hi:[1,0]
	s_nop 0
	v_pk_mul_f32 v[2:3], v[126:127], v[84:85]
	global_store_dwordx4 v[72:73], v[0:3], off
	s_nop 1
	v_pk_mul_f32 v[84:85], v[86:87], v[100:101] op_sel_hi:[1,0]
	v_pk_mul_f32 v[0:1], v[128:129], v[84:85]
	v_pk_mul_f32 v[84:85], v[88:89], v[100:101] op_sel_hi:[1,0]
	s_nop 0
	v_pk_mul_f32 v[2:3], v[130:131], v[84:85]
	global_store_dwordx4 v[72:73], v[0:3], off offset:16
	s_nop 1
	v_pk_mul_f32 v[84:85], v[102:103], v[100:101] op_sel_hi:[1,0]
	v_pk_mul_f32 v[0:1], v[84:85], v[132:133]
	v_pk_mul_f32 v[84:85], v[98:99], v[100:101] op_sel_hi:[1,0]
	s_nop 0
	v_pk_mul_f32 v[2:3], v[84:85], v[134:135]
	global_store_dwordx4 v[72:73], v[0:3], off offset:32
	s_nop 1
	v_pk_mul_f32 v[84:85], v[104:105], v[100:101] op_sel_hi:[1,0]
	v_pk_mul_f32 v[0:1], v[84:85], v[136:137]
	v_pk_mul_f32 v[84:85], v[96:97], v[100:101] op_sel_hi:[1,0]
	s_nop 0
	v_pk_mul_f32 v[2:3], v[84:85], v[138:139]
	global_store_dwordx4 v[72:73], v[0:3], off offset:48
	s_nop 1
	v_mov_b32_e32 v0, v94
	s_andn2_b64 exec, exec, s[10:11]
	s_cbranch_execnz .LBB0_762

.LBB0_770:
	s_cmpk_eq_i32 s56, 0x80
	s_cselect_b64 s[10:11], -1, 0
	ds_bpermute_b32 v6, v97, v96
	s_and_b64 vcc, s[10:11], s[48:49]
	v_cndmask_b32_e32 v94, v0, v98, vcc
	v_ashrrev_i32_e32 v95, 31, v94
	s_and_b32 s10, s56, 0x70
	v_lshlrev_b64 v[94:95], 9, v[94:95]
	v_lshl_add_u64 v[94:95], s[94:95], 0, v[94:95]
	s_lshl_b32 s36, s10, 2
	s_waitcnt lgkmcnt(0)
	v_ashrrev_i32_e32 v7, 31, v6
	v_lshl_add_u64 v[94:95], v[94:95], 0, s[36:37]
	v_lshl_add_u64 v[6:7], v[6:7], 3, s[88:89]
	v_lshl_add_u64 v[94:95], v[94:95], 0, v[144:145]
	global_load_dwordx2 v[6:7], v[6:7], off
	s_nop 0
	global_load_dword v8, v[4:5], off
	global_load_dword v96, v[94:95], off
	s_waitcnt vmcnt(33)
	v_dot8_i32_i4 v9, v20, v1, 0
	v_dot8_i32_i4 v94, v20, v10, 0
	v_dot8_i32_i4 v9, v21, v11, v9
	v_dot8_i32_i4 v94, v21, v12, v94
	v_dot8_i32_i4 v20, v22, v1, 0
	v_dot8_i32_i4 v21, v22, v10, 0
	v_dot8_i32_i4 v20, v23, v11, v20
	v_dot8_i32_i4 v21, v23, v12, v21
	v_lshl_add_u32 v9, v9, 4, v94
	s_add_i32 s56, s56, 16
	s_nop 0
	v_lshl_add_u32 v94, v20, 4, v21
	s_waitcnt vmcnt(32)
	v_dot8_i32_i4 v20, v24, v1, 0
	v_dot8_i32_i4 v21, v24, v10, 0
	v_dot8_i32_i4 v20, v25, v11, v20
	v_dot8_i32_i4 v21, v25, v12, v21
	v_lshl_add_u64 v[4:5], v[4:5], 0, 64
	s_waitcnt vmcnt(2)
	v_mul_f32_e32 v7, v13, v7
	v_lshl_add_u32 v95, v20, 4, v21
	v_dot8_i32_i4 v20, v26, v1, 0
	v_dot8_i32_i4 v21, v26, v10, 0
	v_dot8_i32_i4 v20, v27, v11, v20
	v_dot8_i32_i4 v21, v27, v12, v21
	s_waitcnt vmcnt(0)
	v_readlane_b32 s10, v96, 0
	s_ashr_i32 s11, s10, 31
	v_readlane_b32 s12, v96, 1
	v_lshl_add_u32 v106, v20, 4, v21
	v_dot8_i32_i4 v20, v28, v1, 0
	v_dot8_i32_i4 v21, v28, v10, 0
	v_dot8_i32_i4 v20, v29, v11, v20
	v_dot8_i32_i4 v21, v29, v12, v21
	s_lshl_b64 s[10:11], s[10:11], 9
	s_ashr_i32 s13, s12, 31
	v_readlane_b32 s14, v96, 2
	v_lshl_add_u32 v107, v20, 4, v21
	v_dot8_i32_i4 v20, v30, v1, 0
	v_dot8_i32_i4 v21, v30, v10, 0
	v_dot8_i32_i4 v20, v31, v11, v20
	v_dot8_i32_i4 v21, v31, v12, v21
	s_lshl_b64 s[12:13], s[12:13], 9
	s_ashr_i32 s15, s14, 31
	v_readlane_b32 s16, v96, 3
	v_lshl_add_u32 v108, v20, 4, v21
	v_dot8_i32_i4 v20, v32, v1, 0
	v_dot8_i32_i4 v21, v32, v10, 0
	v_dot8_i32_i4 v20, v33, v11, v20
	v_dot8_i32_i4 v21, v33, v12, v21
	s_lshl_b64 s[14:15], s[14:15], 9
	s_ashr_i32 s17, s16, 31
	s_nop 0
	v_lshl_add_u32 v109, v20, 4, v21
	v_dot8_i32_i4 v20, v34, v1, 0
	v_dot8_i32_i4 v21, v34, v10, 0
	v_dot8_i32_i4 v20, v35, v11, v20
	v_dot8_i32_i4 v21, v35, v12, v21
	v_readlane_b32 s18, v96, 4
	s_add_u32 s66, s12, s62
	s_addc_u32 s67, s13, s63
	global_load_dwordx2 v[22:23], v121, s[66:67]
	v_lshl_add_u32 v110, v20, 4, v21
	v_dot8_i32_i4 v20, v36, v1, 0
	v_dot8_i32_i4 v21, v36, v10, 0
	v_dot8_i32_i4 v20, v37, v11, v20
	v_dot8_i32_i4 v21, v37, v12, v21
	s_lshl_b64 s[16:17], s[16:17], 9
	s_ashr_i32 s19, s18, 31
	v_readlane_b32 s20, v96, 5
	v_lshl_add_u32 v111, v20, 4, v21
	v_dot8_i32_i4 v20, v38, v1, 0
	v_dot8_i32_i4 v21, v38, v10, 0
	v_dot8_i32_i4 v20, v39, v11, v20
	v_dot8_i32_i4 v21, v39, v12, v21
	v_permlane32_swap_b32 v9, v111
	s_nop 1
	v_lshl_add_u32 v112, v20, 4, v21
	v_dot8_i32_i4 v20, v40, v1, 0
	v_dot8_i32_i4 v21, v40, v10, 0
	v_dot8_i32_i4 v20, v41, v11, v20
	v_dot8_i32_i4 v21, v41, v12, v21
	s_waitcnt lgkmcnt(0)
	v_add_u32_e32 v9, v9, v111
	v_permlane32_swap_b32 v94, v112
	v_lshl_add_u32 v113, v20, 4, v21
	v_dot8_i32_i4 v20, v60, v1, 0
	v_dot8_i32_i4 v21, v60, v10, 0
	v_dot8_i32_i4 v20, v61, v11, v20
	v_dot8_i32_i4 v21, v61, v12, v21
	s_waitcnt lgkmcnt(0)
	v_add_u32_e32 v94, v94, v112
	v_permlane32_swap_b32 v95, v113
	v_lshl_add_u32 v114, v20, 4, v21
	v_dot8_i32_i4 v20, v58, v1, 0
	v_dot8_i32_i4 v21, v58, v10, 0
	v_dot8_i32_i4 v20, v59, v11, v20
	v_dot8_i32_i4 v21, v59, v12, v21
	s_waitcnt lgkmcnt(0)
	v_add_u32_e32 v95, v95, v113
	v_permlane32_swap_b32 v106, v114
	v_lshl_add_u32 v115, v20, 4, v21
	v_dot8_i32_i4 v20, v56, v1, 0
	v_dot8_i32_i4 v21, v56, v10, 0
	v_dot8_i32_i4 v20, v57, v11, v20
	v_dot8_i32_i4 v21, v57, v12, v21
	s_waitcnt lgkmcnt(0)
	v_add_u32_e32 v106, v106, v114
	v_permlane32_swap_b32 v107, v115
	v_lshl_add_u32 v116, v20, 4, v21
	v_dot8_i32_i4 v20, v54, v1, 0
	v_dot8_i32_i4 v21, v54, v10, 0
	v_dot8_i32_i4 v20, v55, v11, v20
	v_dot8_i32_i4 v21, v55, v12, v21
	s_waitcnt lgkmcnt(0)
	v_add_u32_e32 v107, v107, v115
	v_permlane32_swap_b32 v108, v116
	v_lshl_add_u32 v117, v20, 4, v21
	v_dot8_i32_i4 v20, v52, v1, 0
	v_dot8_i32_i4 v21, v52, v10, 0
	v_dot8_i32_i4 v20, v53, v11, v20
	v_dot8_i32_i4 v21, v53, v12, v21
	s_waitcnt lgkmcnt(0)
	v_add_u32_e32 v108, v108, v116
	v_permlane32_swap_b32 v109, v117
	v_lshl_add_u32 v118, v20, 4, v21
	s_waitcnt lgkmcnt(0)
	v_add_u32_e32 v109, v109, v117
	v_permlane32_swap_b32 v110, v118
	s_add_u32 s66, s10, s62
	s_addc_u32 s67, s11, s63
	global_load_dwordx2 v[20:21], v121, s[66:67]
	s_add_u32 s66, s14, s62
	s_addc_u32 s67, s15, s63
	global_load_dwordx2 v[24:25], v121, s[66:67]
	s_waitcnt lgkmcnt(0)
	v_add_u32_e32 v110, v110, v118
	v_permlane16_swap_b32 v9, v107
	s_lshl_b64 s[18:19], s[18:19], 9
	s_ashr_i32 s21, s20, 31
	v_readlane_b32 s22, v96, 6
	s_add_u32 s66, s16, s62
	s_addc_u32 s67, s17, s63
	global_load_dwordx2 v[26:27], v121, s[66:67]
	s_waitcnt lgkmcnt(0)
	v_add_u32_e32 v9, v9, v107
	v_permlane16_swap_b32 v94, v108
	s_lshl_b64 s[20:21], s[20:21], 9
	s_ashr_i32 s23, s22, 31
	s_waitcnt lgkmcnt(0)
	v_add_u32_e32 v94, v94, v108
	v_permlane16_swap_b32 v95, v109
	v_readlane_b32 s24, v96, 7
	s_add_u32 s66, s18, s62
	s_addc_u32 s67, s19, s63
	global_load_dwordx2 v[28:29], v121, s[66:67]
	s_waitcnt lgkmcnt(0)
	v_add_u32_e32 v95, v95, v109
	v_permlane16_swap_b32 v106, v110
	s_lshl_b64 s[22:23], s[22:23], 9
	s_ashr_i32 s25, s24, 31
	v_readlane_b32 s26, v96, 8
	s_waitcnt lgkmcnt(0)
	v_add_u32_e32 v106, v106, v110
	v_cndmask_b32_e64 v107, v9, v95, s[44:45]
	v_cndmask_b32_e64 v9, v95, v9, s[44:45]
	s_nop 0
	s_add_u32 s66, s20, s62
	s_addc_u32 s67, s21, s63
	global_load_dwordx2 v[30:31], v121, s[66:67]
	s_lshl_b64 s[24:25], s[24:25], 9
	s_ashr_i32 s27, s26, 31
	s_waitcnt lgkmcnt(0)
	v_add_u32_dpp v9, v107, v9 row_ror:8 row_mask:0xf bank_mask:0xf
	v_cndmask_b32_e64 v95, v94, v106, s[44:45]
	s_nop 1
	v_cndmask_b32_e64 v94, v106, v94, s[44:45]
	v_readlane_b32 s28, v96, 9
	s_add_u32 s66, s22, s62
	s_addc_u32 s67, s23, s63
	global_load_dwordx2 v[32:33], v121, s[66:67]
	s_waitcnt lgkmcnt(0)
	v_add_u32_dpp v94, v95, v94 row_ror:8 row_mask:0xf bank_mask:0xf
	v_cndmask_b32_e64 v95, v9, v94, s[46:47]
	v_cndmask_b32_e64 v9, v94, v9, s[46:47]
	s_nop 0
	v_mov_b32_dpp v94, v95 row_half_mirror row_mask:0xf bank_mask:0xf
	s_nop 1
	s_lshl_b64 s[26:27], s[26:27], 9
	s_ashr_i32 s29, s28, 31
	v_readlane_b32 s30, v96, 10
	s_add_u32 s66, s24, s62
	s_addc_u32 s67, s25, s63
	global_load_dwordx2 v[34:35], v121, s[66:67]
	s_waitcnt lgkmcnt(0)
	v_add_u32_dpp v9, v94, v9 quad_perm:[3,2,1,0] row_mask:0xf bank_mask:0xf
	s_nop 1
	s_lshl_b64 s[28:29], s[28:29], 9
	s_ashr_i32 s31, s30, 31
	v_readlane_b32 s34, v96, 11
	s_waitcnt lgkmcnt(0)
	v_add_u32_dpp v9, v9, v9 quad_perm:[2,3,0,1] row_mask:0xf bank_mask:0xf
	s_nop 1
	s_add_u32 s66, s26, s62
	s_addc_u32 s67, s27, s63
	global_load_dwordx2 v[36:37], v121, s[66:67]
	s_lshl_b64 s[30:31], s[30:31], 9
	s_ashr_i32 s35, s34, 31
	s_waitcnt lgkmcnt(0)
	v_add_u32_dpp v9, v9, v9 quad_perm:[1,0,3,2] row_mask:0xf bank_mask:0xf
	v_cvt_f32_i32_e32 v9, v9
	v_add_f32_e32 v9, v14, v9
	v_mul_f32_e32 v7, v7, v9
	v_mul_f32_e32 v9, 0x3d372713, v7
	v_mul_f32_e32 v9, v7, v9
	v_fma_f32 v9, v7, v9, v7
	v_mul_f32_e32 v9, 0x3fcc422a, v9
	v_mul_f32_e32 v9, 0xbfb8aa3b, v9
	v_exp_f32_e32 v9, v9
	v_lshlrev_b32_e32 v94, 4, v92
	v_readlane_b32 s38, v96, 12
	s_add_u32 s66, s28, s62
	s_addc_u32 s67, s29, s63
	global_load_dwordx2 v[38:39], v121, s[66:67]
	v_add_f32_e32 v9, 1.0, v9
	v_rcp_f32_e32 v9, v9
	s_lshl_b64 s[34:35], s[34:35], 9
	s_ashr_i32 s39, s38, 31
	v_pk_mul_f32 v[6:7], v[6:7], v[8:9]
	v_lshrrev_b32_e32 v9, 4, v92
	v_pk_mul_f32 v[6:7], v[6:7], v[6:7] op_sel:[0,1] op_sel_hi:[1,0]
	v_cvt_f16_f32_e32 v120, v6
	v_and_b32_e32 v8, 0x7070707, v92
	v_readlane_b32 s36, v120, 0
	v_and_b32_e32 v9, 0x7070707, v9
	v_perm_b32 v8, s2, v205, v8
	v_perm_b32 v9, s2, v205, v9
	v_and_or_b32 v8, v94, s4, v8
	v_and_or_b32 v9, v92, s4, v9
	v_perm_b32 v92, v9, v8, s5
	v_perm_b32 v94, v9, v8, s33
	v_perm_b32 v95, v9, v8, s0
	v_perm_b32 v8, v9, v8, s1
	v_pk_fma_f16 v8, v8, s36, v102 op_sel_hi:[1,0,1]
	v_lshrrev_b32_e32 v102, 4, v93
	v_pk_fma_f16 v9, v92, s36, v105 op_sel_hi:[1,0,1]
	v_pk_fma_f16 v92, v94, s36, v104 op_sel_hi:[1,0,1]
	v_pk_fma_f16 v94, v95, s36, v103 op_sel_hi:[1,0,1]
	v_and_b32_e32 v95, 0x7070707, v93
	v_and_b32_e32 v102, 0x7070707, v102
	v_perm_b32 v95, s2, v205, v95
	v_perm_b32 v102, s2, v205, v102
	v_lshlrev_b32_e32 v103, 4, v93
	v_and_or_b32 v95, v103, s4, v95
	v_and_or_b32 v93, v93, s4, v102
	v_perm_b32 v102, v93, v95, s5
	v_perm_b32 v103, v93, v95, s33
	v_perm_b32 v104, v93, v95, s0
	v_perm_b32 v93, v93, v95, s1
	v_pk_fma_f16 v95, v102, s36, v101 op_sel_hi:[1,0,1]
	v_readlane_b32 s59, v120, 4
	v_lshrrev_b32_e32 v101, 4, v90
	v_pk_fma_f16 v100, v103, s36, v100 op_sel_hi:[1,0,1]
	v_pk_fma_f16 v99, v104, s36, v99 op_sel_hi:[1,0,1]
	v_pk_fma_f16 v7, v93, s36, v15 op_sel_hi:[1,0,1]
	v_and_b32_e32 v93, 0x7070707, v90
	v_and_b32_e32 v101, 0x7070707, v101
	v_perm_b32 v93, s2, v205, v93
	v_perm_b32 v101, s2, v205, v101
	v_lshlrev_b32_e32 v102, 4, v90
	v_and_or_b32 v93, v102, s4, v93
	v_and_or_b32 v90, v90, s4, v101
	v_perm_b32 v103, v90, v93, s0
	v_perm_b32 v101, v90, v93, s5
	v_perm_b32 v102, v90, v93, s33
	v_perm_b32 v90, v90, v93, s1
	v_pk_fma_f16 v93, v103, s59, v94 op_sel_hi:[1,0,1]
	v_lshrrev_b32_e32 v94, 4, v91
	v_pk_fma_f16 v8, v90, s59, v8 op_sel_hi:[1,0,1]
	v_and_b32_e32 v90, 0x7070707, v91
	v_and_b32_e32 v94, 0x7070707, v94
	v_pk_fma_f16 v9, v101, s59, v9 op_sel_hi:[1,0,1]
	v_perm_b32 v90, s2, v205, v90
	v_perm_b32 v94, s2, v205, v94
	v_lshlrev_b32_e32 v101, 4, v91
	v_and_or_b32 v90, v101, s4, v90
	v_and_or_b32 v91, v91, s4, v94
	v_pk_fma_f16 v92, v102, s59, v92 op_sel_hi:[1,0,1]
	v_perm_b32 v94, v91, v90, s5
	v_perm_b32 v102, v91, v90, s0
	v_perm_b32 v101, v91, v90, s33
	v_perm_b32 v90, v91, v90, s1
	v_pk_fma_f16 v91, v94, s59, v95 op_sel_hi:[1,0,1]
	v_pk_fma_f16 v95, v102, s59, v99 op_sel_hi:[1,0,1]
	v_readlane_b32 s60, v120, 8
	v_lshrrev_b32_e32 v99, 4, v88
	v_pk_fma_f16 v94, v101, s59, v100 op_sel_hi:[1,0,1]
	v_pk_fma_f16 v7, v90, s59, v7 op_sel_hi:[1,0,1]
	v_and_b32_e32 v90, 0x7070707, v88
	v_and_b32_e32 v99, 0x7070707, v99
	v_perm_b32 v90, s2, v205, v90
	v_perm_b32 v99, s2, v205, v99
	v_lshlrev_b32_e32 v100, 4, v88
	v_and_or_b32 v90, v100, s4, v90
	v_and_or_b32 v88, v88, s4, v99
	v_perm_b32 v100, v88, v90, s33
	v_perm_b32 v101, v88, v90, s0
	v_perm_b32 v99, v88, v90, s5
	v_perm_b32 v88, v88, v90, s1
	v_pk_fma_f16 v90, v100, s60, v92 op_sel_hi:[1,0,1]
	v_pk_fma_f16 v92, v101, s60, v93 op_sel_hi:[1,0,1]
	v_lshrrev_b32_e32 v93, 4, v89
	v_pk_fma_f16 v8, v88, s60, v8 op_sel_hi:[1,0,1]
	v_and_b32_e32 v88, 0x7070707, v89
	v_and_b32_e32 v93, 0x7070707, v93
	v_pk_fma_f16 v9, v99, s60, v9 op_sel_hi:[1,0,1]
	v_perm_b32 v88, s2, v205, v88
	v_perm_b32 v93, s2, v205, v93
	v_lshlrev_b32_e32 v99, 4, v89
	v_and_or_b32 v88, v99, s4, v88
	v_and_or_b32 v89, v89, s4, v93
	v_perm_b32 v93, v89, v88, s5
	v_perm_b32 v99, v89, v88, s33
	v_perm_b32 v100, v89, v88, s0
	v_perm_b32 v88, v89, v88, s1
	v_pk_fma_f16 v89, v93, s60, v91 op_sel_hi:[1,0,1]
	v_pk_fma_f16 v91, v99, s60, v94 op_sel_hi:[1,0,1]
	v_readlane_b32 s36, v120, 12
	v_lshrrev_b32_e32 v94, 4, v86
	v_pk_fma_f16 v93, v100, s60, v95 op_sel_hi:[1,0,1]
	v_pk_fma_f16 v7, v88, s60, v7 op_sel_hi:[1,0,1]
	v_and_b32_e32 v88, 0x7070707, v86
	v_and_b32_e32 v94, 0x7070707, v94
	v_perm_b32 v88, s2, v205, v88
	v_perm_b32 v94, s2, v205, v94
	v_lshlrev_b32_e32 v95, 4, v86
	v_and_or_b32 v88, v95, s4, v88
	v_and_or_b32 v86, v86, s4, v94
	v_perm_b32 v95, v86, v88, s33
	v_perm_b32 v99, v86, v88, s0
	v_perm_b32 v94, v86, v88, s5
	v_perm_b32 v86, v86, v88, s1
	v_pk_fma_f16 v88, v95, s36, v90 op_sel_hi:[1,0,1]
	v_pk_fma_f16 v90, v99, s36, v92 op_sel_hi:[1,0,1]
	v_lshrrev_b32_e32 v92, 4, v87
	v_pk_fma_f16 v8, v86, s36, v8 op_sel_hi:[1,0,1]
	v_and_b32_e32 v86, 0x7070707, v87
	v_and_b32_e32 v92, 0x7070707, v92
	v_pk_fma_f16 v9, v94, s36, v9 op_sel_hi:[1,0,1]
	v_perm_b32 v86, s2, v205, v86
	v_perm_b32 v92, s2, v205, v92
	v_lshlrev_b32_e32 v94, 4, v87
	v_and_or_b32 v86, v94, s4, v86
	v_and_or_b32 v87, v87, s4, v92
	v_perm_b32 v92, v87, v86, s5
	v_perm_b32 v94, v87, v86, s33
	v_perm_b32 v95, v87, v86, s0
	v_perm_b32 v86, v87, v86, s1
	v_pk_fma_f16 v87, v92, s36, v89 op_sel_hi:[1,0,1]
	v_readlane_b32 s59, v120, 16
	v_lshrrev_b32_e32 v92, 4, v84
	v_pk_fma_f16 v89, v94, s36, v91 op_sel_hi:[1,0,1]
	v_pk_fma_f16 v91, v95, s36, v93 op_sel_hi:[1,0,1]
	v_pk_fma_f16 v7, v86, s36, v7 op_sel_hi:[1,0,1]
	v_and_b32_e32 v86, 0x7070707, v84
	v_and_b32_e32 v92, 0x7070707, v92
	v_perm_b32 v86, s2, v205, v86
	v_perm_b32 v92, s2, v205, v92
	v_lshlrev_b32_e32 v93, 4, v84
	v_and_or_b32 v86, v93, s4, v86
	v_and_or_b32 v84, v84, s4, v92
	v_perm_b32 v93, v84, v86, s33
	v_perm_b32 v94, v84, v86, s0
	v_perm_b32 v92, v84, v86, s5
	v_perm_b32 v84, v84, v86, s1
	v_pk_fma_f16 v86, v93, s59, v88 op_sel_hi:[1,0,1]
	v_pk_fma_f16 v88, v94, s59, v90 op_sel_hi:[1,0,1]
	v_lshrrev_b32_e32 v90, 4, v85
	v_pk_fma_f16 v8, v84, s59, v8 op_sel_hi:[1,0,1]
	v_and_b32_e32 v84, 0x7070707, v85
	v_and_b32_e32 v90, 0x7070707, v90
	v_pk_fma_f16 v9, v92, s59, v9 op_sel_hi:[1,0,1]
	v_perm_b32 v84, s2, v205, v84
	v_perm_b32 v90, s2, v205, v90
	v_lshlrev_b32_e32 v92, 4, v85
	v_and_or_b32 v84, v92, s4, v84
	v_and_or_b32 v85, v85, s4, v90
	v_perm_b32 v90, v85, v84, s5
	v_perm_b32 v92, v85, v84, s33
	v_perm_b32 v93, v85, v84, s0
	v_perm_b32 v84, v85, v84, s1
	v_pk_fma_f16 v85, v90, s59, v87 op_sel_hi:[1,0,1]
	v_readlane_b32 s60, v120, 20
	v_lshrrev_b32_e32 v90, 4, v82
	v_pk_fma_f16 v87, v92, s59, v89 op_sel_hi:[1,0,1]
	v_pk_fma_f16 v89, v93, s59, v91 op_sel_hi:[1,0,1]
	v_pk_fma_f16 v7, v84, s59, v7 op_sel_hi:[1,0,1]
	v_and_b32_e32 v84, 0x7070707, v82
	v_and_b32_e32 v90, 0x7070707, v90
	v_perm_b32 v84, s2, v205, v84
	v_perm_b32 v90, s2, v205, v90
	v_lshlrev_b32_e32 v91, 4, v82
	v_and_or_b32 v84, v91, s4, v84
	v_and_or_b32 v82, v82, s4, v90
	v_perm_b32 v91, v82, v84, s33
	v_perm_b32 v92, v82, v84, s0
	v_perm_b32 v90, v82, v84, s5
	v_perm_b32 v82, v82, v84, s1
	v_pk_fma_f16 v84, v91, s60, v86 op_sel_hi:[1,0,1]
	v_pk_fma_f16 v86, v92, s60, v88 op_sel_hi:[1,0,1]
	v_lshrrev_b32_e32 v88, 4, v83
	v_pk_fma_f16 v8, v82, s60, v8 op_sel_hi:[1,0,1]
	v_and_b32_e32 v82, 0x7070707, v83
	v_and_b32_e32 v88, 0x7070707, v88
	v_pk_fma_f16 v9, v90, s60, v9 op_sel_hi:[1,0,1]
	v_perm_b32 v82, s2, v205, v82
	v_perm_b32 v88, s2, v205, v88
	v_lshlrev_b32_e32 v90, 4, v83
	v_and_or_b32 v82, v90, s4, v82
	v_and_or_b32 v83, v83, s4, v88
	v_perm_b32 v88, v83, v82, s5
	v_perm_b32 v90, v83, v82, s33
	v_perm_b32 v91, v83, v82, s0
	v_perm_b32 v82, v83, v82, s1
	v_pk_fma_f16 v83, v88, s60, v85 op_sel_hi:[1,0,1]
	v_readlane_b32 s36, v120, 24
	v_lshrrev_b32_e32 v88, 4, v80
	v_pk_fma_f16 v85, v90, s60, v87 op_sel_hi:[1,0,1]
	v_pk_fma_f16 v87, v91, s60, v89 op_sel_hi:[1,0,1]
	v_pk_fma_f16 v7, v82, s60, v7 op_sel_hi:[1,0,1]
	v_and_b32_e32 v82, 0x7070707, v80
	v_and_b32_e32 v88, 0x7070707, v88
	v_perm_b32 v82, s2, v205, v82
	v_perm_b32 v88, s2, v205, v88
	v_lshlrev_b32_e32 v89, 4, v80
	v_and_or_b32 v82, v89, s4, v82
	v_and_or_b32 v80, v80, s4, v88
	v_perm_b32 v89, v80, v82, s33
	v_perm_b32 v90, v80, v82, s0
	v_perm_b32 v88, v80, v82, s5
	v_perm_b32 v80, v80, v82, s1
	v_pk_fma_f16 v82, v89, s36, v84 op_sel_hi:[1,0,1]
	v_pk_fma_f16 v84, v90, s36, v86 op_sel_hi:[1,0,1]
	v_lshrrev_b32_e32 v86, 4, v81
	v_pk_fma_f16 v8, v80, s36, v8 op_sel_hi:[1,0,1]
	v_and_b32_e32 v80, 0x7070707, v81
	v_and_b32_e32 v86, 0x7070707, v86
	v_pk_fma_f16 v9, v88, s36, v9 op_sel_hi:[1,0,1]
	v_perm_b32 v80, s2, v205, v80
	v_perm_b32 v86, s2, v205, v86
	v_lshlrev_b32_e32 v88, 4, v81
	v_and_or_b32 v80, v88, s4, v80
	v_and_or_b32 v81, v81, s4, v86
	v_perm_b32 v86, v81, v80, s5
	v_perm_b32 v88, v81, v80, s33
	v_perm_b32 v89, v81, v80, s0
	v_perm_b32 v80, v81, v80, s1
	v_pk_fma_f16 v81, v86, s36, v83 op_sel_hi:[1,0,1]
	v_readlane_b32 s59, v120, 28
	v_lshrrev_b32_e32 v86, 4, v78
	v_pk_fma_f16 v83, v88, s36, v85 op_sel_hi:[1,0,1]
	v_pk_fma_f16 v85, v89, s36, v87 op_sel_hi:[1,0,1]
	v_pk_fma_f16 v7, v80, s36, v7 op_sel_hi:[1,0,1]
	v_and_b32_e32 v80, 0x7070707, v78
	v_and_b32_e32 v86, 0x7070707, v86
	v_perm_b32 v80, s2, v205, v80
	v_perm_b32 v86, s2, v205, v86
	v_lshlrev_b32_e32 v87, 4, v78
	v_and_or_b32 v80, v87, s4, v80
	v_and_or_b32 v78, v78, s4, v86
	v_perm_b32 v87, v78, v80, s33
	v_perm_b32 v88, v78, v80, s0
	v_perm_b32 v86, v78, v80, s5
	v_perm_b32 v78, v78, v80, s1
	v_pk_fma_f16 v80, v87, s59, v82 op_sel_hi:[1,0,1]
	v_pk_fma_f16 v82, v88, s59, v84 op_sel_hi:[1,0,1]
	v_lshrrev_b32_e32 v84, 4, v79
	v_pk_fma_f16 v8, v78, s59, v8 op_sel_hi:[1,0,1]
	v_and_b32_e32 v78, 0x7070707, v79
	v_and_b32_e32 v84, 0x7070707, v84
	v_pk_fma_f16 v9, v86, s59, v9 op_sel_hi:[1,0,1]
	v_perm_b32 v78, s2, v205, v78
	v_perm_b32 v84, s2, v205, v84
	v_lshlrev_b32_e32 v86, 4, v79
	v_and_or_b32 v78, v86, s4, v78
	v_and_or_b32 v79, v79, s4, v84
	v_perm_b32 v84, v79, v78, s5
	v_perm_b32 v86, v79, v78, s33
	v_perm_b32 v87, v79, v78, s0
	v_perm_b32 v78, v79, v78, s1
	v_pk_fma_f16 v79, v84, s59, v81 op_sel_hi:[1,0,1]
	v_readlane_b32 s60, v120, 32
	v_lshrrev_b32_e32 v84, 4, v76
	v_pk_fma_f16 v81, v86, s59, v83 op_sel_hi:[1,0,1]
	v_pk_fma_f16 v83, v87, s59, v85 op_sel_hi:[1,0,1]
	v_pk_fma_f16 v7, v78, s59, v7 op_sel_hi:[1,0,1]
	v_and_b32_e32 v78, 0x7070707, v76
	v_and_b32_e32 v84, 0x7070707, v84
	v_perm_b32 v78, s2, v205, v78
	v_perm_b32 v84, s2, v205, v84
	v_lshlrev_b32_e32 v85, 4, v76
	v_and_or_b32 v78, v85, s4, v78
	v_and_or_b32 v76, v76, s4, v84
	v_perm_b32 v85, v76, v78, s33
	v_perm_b32 v86, v76, v78, s0
	v_perm_b32 v84, v76, v78, s5
	v_perm_b32 v76, v76, v78, s1
	v_pk_fma_f16 v78, v85, s60, v80 op_sel_hi:[1,0,1]
	v_pk_fma_f16 v80, v86, s60, v82 op_sel_hi:[1,0,1]
	v_lshrrev_b32_e32 v82, 4, v77
	v_pk_fma_f16 v8, v76, s60, v8 op_sel_hi:[1,0,1]
	v_and_b32_e32 v76, 0x7070707, v77
	v_and_b32_e32 v82, 0x7070707, v82
	v_pk_fma_f16 v9, v84, s60, v9 op_sel_hi:[1,0,1]
	v_perm_b32 v76, s2, v205, v76
	v_perm_b32 v82, s2, v205, v82
	v_lshlrev_b32_e32 v84, 4, v77
	v_and_or_b32 v76, v84, s4, v76
	v_and_or_b32 v77, v77, s4, v82
	v_perm_b32 v82, v77, v76, s5
	v_perm_b32 v84, v77, v76, s33
	v_perm_b32 v85, v77, v76, s0
	v_perm_b32 v76, v77, v76, s1
	v_pk_fma_f16 v77, v82, s60, v79 op_sel_hi:[1,0,1]
	v_readlane_b32 s36, v120, 36
	v_lshrrev_b32_e32 v82, 4, v70
	v_pk_fma_f16 v79, v84, s60, v81 op_sel_hi:[1,0,1]
	v_pk_fma_f16 v81, v85, s60, v83 op_sel_hi:[1,0,1]
	v_pk_fma_f16 v7, v76, s60, v7 op_sel_hi:[1,0,1]
	v_and_b32_e32 v76, 0x7070707, v70
	v_and_b32_e32 v82, 0x7070707, v82
	v_perm_b32 v76, s2, v205, v76
	v_perm_b32 v82, s2, v205, v82
	v_lshlrev_b32_e32 v83, 4, v70
	v_and_or_b32 v76, v83, s4, v76
	v_and_or_b32 v70, v70, s4, v82
	v_perm_b32 v83, v70, v76, s33
	v_perm_b32 v84, v70, v76, s0
	v_perm_b32 v82, v70, v76, s5
	v_perm_b32 v70, v70, v76, s1
	v_pk_fma_f16 v76, v83, s36, v78 op_sel_hi:[1,0,1]
	v_pk_fma_f16 v78, v84, s36, v80 op_sel_hi:[1,0,1]
	v_lshrrev_b32_e32 v80, 4, v71
	v_pk_fma_f16 v8, v70, s36, v8 op_sel_hi:[1,0,1]
	v_and_b32_e32 v70, 0x7070707, v71
	v_and_b32_e32 v80, 0x7070707, v80
	v_pk_fma_f16 v9, v82, s36, v9 op_sel_hi:[1,0,1]
	v_perm_b32 v70, s2, v205, v70
	v_perm_b32 v80, s2, v205, v80
	v_lshlrev_b32_e32 v82, 4, v71
	v_and_or_b32 v70, v82, s4, v70
	v_and_or_b32 v71, v71, s4, v80
	v_perm_b32 v80, v71, v70, s5
	v_perm_b32 v82, v71, v70, s33
	v_perm_b32 v83, v71, v70, s0
	v_perm_b32 v70, v71, v70, s1
	v_pk_fma_f16 v71, v80, s36, v77 op_sel_hi:[1,0,1]
	v_readlane_b32 s59, v120, 40
	v_lshrrev_b32_e32 v80, 4, v66
	v_pk_fma_f16 v77, v82, s36, v79 op_sel_hi:[1,0,1]
	v_pk_fma_f16 v79, v83, s36, v81 op_sel_hi:[1,0,1]
	v_pk_fma_f16 v7, v70, s36, v7 op_sel_hi:[1,0,1]
	v_and_b32_e32 v70, 0x7070707, v66
	v_and_b32_e32 v80, 0x7070707, v80
	v_perm_b32 v70, s2, v205, v70
	v_perm_b32 v80, s2, v205, v80
	v_lshlrev_b32_e32 v81, 4, v66
	v_and_or_b32 v70, v81, s4, v70
	v_and_or_b32 v66, v66, s4, v80
	v_perm_b32 v81, v66, v70, s33
	v_perm_b32 v82, v66, v70, s0
	v_perm_b32 v80, v66, v70, s5
	v_perm_b32 v66, v66, v70, s1
	v_pk_fma_f16 v70, v81, s59, v76 op_sel_hi:[1,0,1]
	v_pk_fma_f16 v76, v82, s59, v78 op_sel_hi:[1,0,1]
	v_lshrrev_b32_e32 v78, 4, v67
	v_pk_fma_f16 v8, v66, s59, v8 op_sel_hi:[1,0,1]
	v_and_b32_e32 v66, 0x7070707, v67
	v_and_b32_e32 v78, 0x7070707, v78
	v_pk_fma_f16 v9, v80, s59, v9 op_sel_hi:[1,0,1]
	v_perm_b32 v66, s2, v205, v66
	v_perm_b32 v78, s2, v205, v78
	v_lshlrev_b32_e32 v80, 4, v67
	v_and_or_b32 v66, v80, s4, v66
	v_and_or_b32 v67, v67, s4, v78
	v_perm_b32 v78, v67, v66, s5
	v_perm_b32 v80, v67, v66, s33
	v_perm_b32 v81, v67, v66, s0
	v_perm_b32 v66, v67, v66, s1
	v_pk_fma_f16 v67, v78, s59, v71 op_sel_hi:[1,0,1]
	v_readlane_b32 s60, v120, 44
	v_lshrrev_b32_e32 v78, 4, v72
	v_pk_fma_f16 v71, v80, s59, v77 op_sel_hi:[1,0,1]
	v_pk_fma_f16 v77, v81, s59, v79 op_sel_hi:[1,0,1]
	v_pk_fma_f16 v7, v66, s59, v7 op_sel_hi:[1,0,1]
	v_and_b32_e32 v66, 0x7070707, v72
	v_and_b32_e32 v78, 0x7070707, v78
	v_perm_b32 v66, s2, v205, v66
	v_perm_b32 v78, s2, v205, v78
	v_lshlrev_b32_e32 v79, 4, v72
	v_and_or_b32 v66, v79, s4, v66
	v_and_or_b32 v72, v72, s4, v78
	v_perm_b32 v80, v72, v66, s0
	v_perm_b32 v78, v72, v66, s5
	v_perm_b32 v79, v72, v66, s33
	v_perm_b32 v66, v72, v66, s1
	v_pk_fma_f16 v72, v80, s60, v76 op_sel_hi:[1,0,1]
	v_lshrrev_b32_e32 v76, 4, v73
	v_pk_fma_f16 v8, v66, s60, v8 op_sel_hi:[1,0,1]
	v_and_b32_e32 v66, 0x7070707, v73
	v_and_b32_e32 v76, 0x7070707, v76
	v_pk_fma_f16 v9, v78, s60, v9 op_sel_hi:[1,0,1]
	v_perm_b32 v66, s2, v205, v66
	v_perm_b32 v76, s2, v205, v76
	v_lshlrev_b32_e32 v78, 4, v73
	v_and_or_b32 v66, v78, s4, v66
	v_and_or_b32 v73, v73, s4, v76
	v_perm_b32 v76, v73, v66, s5
	v_pk_fma_f16 v70, v79, s60, v70 op_sel_hi:[1,0,1]
	v_perm_b32 v78, v73, v66, s33
	v_perm_b32 v79, v73, v66, s0
	v_perm_b32 v66, v73, v66, s1
	v_pk_fma_f16 v67, v76, s60, v67 op_sel_hi:[1,0,1]
	v_readlane_b32 s36, v120, 48
	v_lshrrev_b32_e32 v76, 4, v68
	v_pk_fma_f16 v71, v78, s60, v71 op_sel_hi:[1,0,1]
	v_pk_fma_f16 v73, v79, s60, v77 op_sel_hi:[1,0,1]
	v_pk_fma_f16 v7, v66, s60, v7 op_sel_hi:[1,0,1]
	v_and_b32_e32 v66, 0x7070707, v68
	v_and_b32_e32 v76, 0x7070707, v76
	v_perm_b32 v66, s2, v205, v66
	v_perm_b32 v76, s2, v205, v76
	v_lshlrev_b32_e32 v77, 4, v68
	v_and_or_b32 v66, v77, s4, v66
	v_and_or_b32 v68, v68, s4, v76
	v_perm_b32 v77, v68, v66, s33
	v_perm_b32 v78, v68, v66, s0
	v_perm_b32 v76, v68, v66, s5
	v_perm_b32 v66, v68, v66, s1
	v_pk_fma_f16 v68, v77, s36, v70 op_sel_hi:[1,0,1]
	v_pk_fma_f16 v70, v78, s36, v72 op_sel_hi:[1,0,1]
	v_lshrrev_b32_e32 v72, 4, v69
	v_pk_fma_f16 v8, v66, s36, v8 op_sel_hi:[1,0,1]
	v_and_b32_e32 v66, 0x7070707, v69
	v_and_b32_e32 v72, 0x7070707, v72
	v_pk_fma_f16 v9, v76, s36, v9 op_sel_hi:[1,0,1]
	v_perm_b32 v66, s2, v205, v66
	v_perm_b32 v72, s2, v205, v72
	v_lshlrev_b32_e32 v76, 4, v69
	v_and_or_b32 v66, v76, s4, v66
	v_and_or_b32 v69, v69, s4, v72
	v_perm_b32 v72, v69, v66, s5
	v_perm_b32 v76, v69, v66, s33
	v_perm_b32 v77, v69, v66, s0
	v_perm_b32 v66, v69, v66, s1
	v_pk_fma_f16 v67, v72, s36, v67 op_sel_hi:[1,0,1]
	v_readlane_b32 s59, v120, 52
	v_lshrrev_b32_e32 v72, 4, v64
	v_pk_fma_f16 v69, v76, s36, v71 op_sel_hi:[1,0,1]
	v_pk_fma_f16 v71, v77, s36, v73 op_sel_hi:[1,0,1]
	v_pk_fma_f16 v7, v66, s36, v7 op_sel_hi:[1,0,1]
	v_and_b32_e32 v66, 0x7070707, v64
	v_and_b32_e32 v72, 0x7070707, v72
	v_perm_b32 v66, s2, v205, v66
	v_perm_b32 v72, s2, v205, v72
	v_lshlrev_b32_e32 v73, 4, v64
	v_and_or_b32 v66, v73, s4, v66
	v_and_or_b32 v64, v64, s4, v72
	v_perm_b32 v73, v64, v66, s33
	v_perm_b32 v76, v64, v66, s0
	v_perm_b32 v72, v64, v66, s5
	v_perm_b32 v64, v64, v66, s1
	v_pk_fma_f16 v66, v73, s59, v68 op_sel_hi:[1,0,1]
	v_pk_fma_f16 v68, v76, s59, v70 op_sel_hi:[1,0,1]
	v_lshrrev_b32_e32 v70, 4, v65
	v_pk_fma_f16 v8, v64, s59, v8 op_sel_hi:[1,0,1]
	v_and_b32_e32 v64, 0x7070707, v65
	v_and_b32_e32 v70, 0x7070707, v70
	v_pk_fma_f16 v9, v72, s59, v9 op_sel_hi:[1,0,1]
	v_perm_b32 v64, s2, v205, v64
	v_perm_b32 v70, s2, v205, v70
	v_lshlrev_b32_e32 v72, 4, v65
	v_and_or_b32 v64, v72, s4, v64
	v_and_or_b32 v65, v65, s4, v70
	v_perm_b32 v70, v65, v64, s5
	v_perm_b32 v72, v65, v64, s33
	v_perm_b32 v73, v65, v64, s0
	v_perm_b32 v64, v65, v64, s1
	v_pk_fma_f16 v65, v70, s59, v67 op_sel_hi:[1,0,1]
	v_readlane_b32 s60, v120, 56
	v_lshrrev_b32_e32 v70, 4, v62
	v_pk_fma_f16 v67, v72, s59, v69 op_sel_hi:[1,0,1]
	v_pk_fma_f16 v69, v73, s59, v71 op_sel_hi:[1,0,1]
	v_pk_fma_f16 v7, v64, s59, v7 op_sel_hi:[1,0,1]
	v_and_b32_e32 v64, 0x7070707, v62
	v_and_b32_e32 v70, 0x7070707, v70
	v_perm_b32 v64, s2, v205, v64
	v_perm_b32 v70, s2, v205, v70
	v_lshlrev_b32_e32 v71, 4, v62
	v_and_or_b32 v64, v71, s4, v64
	v_and_or_b32 v62, v62, s4, v70
	v_perm_b32 v71, v62, v64, s33
	v_perm_b32 v72, v62, v64, s0
	v_perm_b32 v70, v62, v64, s5
	v_perm_b32 v62, v62, v64, s1
	v_pk_fma_f16 v64, v71, s60, v66 op_sel_hi:[1,0,1]
	v_pk_fma_f16 v66, v72, s60, v68 op_sel_hi:[1,0,1]
	v_lshrrev_b32_e32 v68, 4, v63
	v_pk_fma_f16 v8, v62, s60, v8 op_sel_hi:[1,0,1]
	v_and_b32_e32 v62, 0x7070707, v63
	v_and_b32_e32 v68, 0x7070707, v68
	v_pk_fma_f16 v9, v70, s60, v9 op_sel_hi:[1,0,1]
	v_perm_b32 v62, s2, v205, v62
	v_perm_b32 v68, s2, v205, v68
	v_lshlrev_b32_e32 v70, 4, v63
	v_and_or_b32 v62, v70, s4, v62
	v_and_or_b32 v63, v63, s4, v68
	v_perm_b32 v68, v63, v62, s5
	v_perm_b32 v70, v63, v62, s33
	v_perm_b32 v71, v63, v62, s0
	v_perm_b32 v62, v63, v62, s1
	v_pk_fma_f16 v7, v62, s60, v7 op_sel_hi:[1,0,1]
	v_readlane_b32 s36, v120, 60
	v_lshrrev_b32_e32 v62, 4, v50
	v_pk_fma_f16 v63, v68, s60, v65 op_sel_hi:[1,0,1]
	v_pk_fma_f16 v65, v70, s60, v67 op_sel_hi:[1,0,1]
	v_pk_fma_f16 v67, v71, s60, v69 op_sel_hi:[1,0,1]
	v_and_b32_e32 v15, 0x7070707, v50
	v_and_b32_e32 v62, 0x7070707, v62
	v_perm_b32 v15, s2, v205, v15
	v_perm_b32 v62, s2, v205, v62
	v_lshlrev_b32_e32 v68, 4, v50
	v_and_or_b32 v15, v68, s4, v15
	v_and_or_b32 v50, v50, s4, v62
	v_perm_b32 v62, v50, v15, s5
	v_perm_b32 v68, v50, v15, s33
	v_perm_b32 v69, v50, v15, s0
	v_perm_b32 v15, v50, v15, s1
	v_pk_fma_f16 v105, v62, s36, v9 op_sel_hi:[1,0,1]
	v_lshrrev_b32_e32 v9, 4, v51
	v_pk_fma_f16 v102, v15, s36, v8 op_sel_hi:[1,0,1]
	v_and_b32_e32 v8, 0x7070707, v51
	v_and_b32_e32 v9, 0x7070707, v9
	v_perm_b32 v8, s2, v205, v8
	v_perm_b32 v9, s2, v205, v9
	v_lshlrev_b32_e32 v15, 4, v51
	v_and_or_b32 v8, v15, s4, v8
	v_and_or_b32 v9, v51, s4, v9
	v_perm_b32 v15, v9, v8, s5
	v_perm_b32 v50, v9, v8, s33
	v_perm_b32 v51, v9, v8, s0
	v_perm_b32 v8, v9, v8, s1
	v_pk_fma_f16 v104, v68, s36, v64 op_sel_hi:[1,0,1]
	v_pk_fma_f16 v103, v69, s36, v66 op_sel_hi:[1,0,1]
	v_pk_fma_f16 v101, v15, s36, v63 op_sel_hi:[1,0,1]
	v_pk_fma_f16 v100, v50, s36, v65 op_sel_hi:[1,0,1]
	v_pk_fma_f16 v99, v51, s36, v67 op_sel_hi:[1,0,1]
	v_pk_fma_f16 v15, v8, s36, v7 op_sel_hi:[1,0,1]
	s_add_u32 s66, s10, s64
	s_addc_u32 s67, s11, s65
	global_load_dwordx2 v[92:93], v121, s[66:67]
	s_add_u32 s66, s12, s64
	s_addc_u32 s67, s13, s65
	global_load_dwordx2 v[90:91], v121, s[66:67]
	s_add_u32 s66, s14, s64
	s_addc_u32 s67, s15, s65
	global_load_dwordx2 v[88:89], v121, s[66:67]
	s_add_u32 s66, s16, s64
	s_addc_u32 s67, s17, s65
	global_load_dwordx2 v[86:87], v121, s[66:67]
	s_add_u32 s66, s18, s64
	s_addc_u32 s67, s19, s65
	global_load_dwordx2 v[84:85], v121, s[66:67]
	s_add_u32 s66, s20, s64
	s_addc_u32 s67, s21, s65
	global_load_dwordx2 v[82:83], v121, s[66:67]
	s_add_u32 s66, s22, s64
	s_addc_u32 s67, s23, s65
	global_load_dwordx2 v[80:81], v121, s[66:67]
	s_add_u32 s66, s24, s64
	s_addc_u32 s67, s25, s65
	global_load_dwordx2 v[78:79], v121, s[66:67]
	s_add_u32 s66, s26, s64
	s_addc_u32 s67, s27, s65
	global_load_dwordx2 v[76:77], v121, s[66:67]
	v_readlane_b32 s50, v96, 13
	s_add_u32 s66, s28, s64
	s_addc_u32 s67, s29, s65
	global_load_dwordx2 v[70:71], v121, s[66:67]
	s_add_u32 s66, s30, s62
	s_addc_u32 s67, s31, s63
	global_load_dwordx2 v[40:41], v121, s[66:67]
	s_lshl_b64 s[38:39], s[38:39], 9
	s_ashr_i32 s51, s50, 31
	v_readlane_b32 s52, v96, 14
	s_add_u32 s66, s30, s64
	s_addc_u32 s67, s31, s65
	global_load_dwordx2 v[66:67], v121, s[66:67]
	s_add_u32 s66, s34, s62
	s_addc_u32 s67, s35, s63
	global_load_dwordx2 v[60:61], v121, s[66:67]
	s_add_u32 s66, s34, s64
	s_addc_u32 s67, s35, s65
	global_load_dwordx2 v[72:73], v121, s[66:67]
	s_lshl_b64 s[50:51], s[50:51], 9
	s_ashr_i32 s53, s52, 31
	v_readlane_b32 s54, v96, 15
	s_add_u32 s66, s38, s62
	s_addc_u32 s67, s39, s63
	global_load_dwordx2 v[58:59], v121, s[66:67]
	s_add_u32 s66, s38, s64
	s_addc_u32 s67, s39, s65
	global_load_dwordx2 v[68:69], v121, s[66:67]
	s_lshl_b64 s[52:53], s[52:53], 9
	s_ashr_i32 s55, s54, 31
	s_add_u32 s66, s50, s62
	s_addc_u32 s67, s51, s63
	global_load_dwordx2 v[56:57], v121, s[66:67]
	s_add_u32 s66, s50, s64
	s_addc_u32 s67, s51, s65
	global_load_dwordx2 v[64:65], v121, s[66:67]
	s_lshl_b64 s[54:55], s[54:55], 9
	s_add_u32 s66, s52, s62
	s_addc_u32 s67, s53, s63
	global_load_dwordx2 v[54:55], v121, s[66:67]
	s_add_u32 s66, s52, s64
	s_addc_u32 s67, s53, s65
	global_load_dwordx2 v[62:63], v121, s[66:67]
	s_add_u32 s66, s54, s62
	s_addc_u32 s67, s55, s63
	global_load_dwordx2 v[52:53], v121, s[66:67]
	s_add_u32 s66, s54, s64
	s_addc_u32 s67, s55, s65
	global_load_dwordx2 v[50:51], v121, s[66:67]
	s_cmpk_eq_i32 s56, 0x90
	s_cbranch_scc0 .LBB0_770
	v_lshl_add_u64 v[94:95], v[2:3], 2, v[44:45]
	v_mov_b32_e32 v106, v208
	v_mov_b32_e32 v107, v209
	v_mov_b32_e32 v108, v210
	v_mov_b32_e32 v109, v211
	v_mov_b32_e32 v8, v212
	v_mov_b32_e32 v9, v213
	v_mov_b32_e32 v10, v214
	v_mov_b32_e32 v11, v215
	v_mov_b32_e32 v4, v216
	v_mov_b32_e32 v5, v217
	v_mov_b32_e32 v6, v218
	v_mov_b32_e32 v7, v219
	v_mov_b32_e32 v0, v220
	v_mov_b32_e32 v1, v221
	v_mov_b32_e32 v2, v222
	v_mov_b32_e32 v3, v223
	v_cvt_f32_f16_sdwa v13, v105 dst_sel:DWORD dst_unused:UNUSED_PAD src0_sel:WORD_1
	v_cvt_f32_f16_e32 v12, v105
	s_mov_b32 s12, 0x800000
	v_readlane_b32 s10, v255, 5
	v_readlane_b32 s11, v255, 6
	v_pk_add_f32 v[0:1], v[0:1], v[12:13]
	v_cvt_f32_f16_sdwa v13, v104 dst_sel:DWORD dst_unused:UNUSED_PAD src0_sel:WORD_1
	v_cvt_f32_f16_e32 v12, v104
	v_lshl_add_u64 v[48:49], v[48:49], 0, s[10:11]
	v_pk_add_f32 v[2:3], v[2:3], v[12:13]
	v_cvt_f32_f16_sdwa v13, v103 dst_sel:DWORD dst_unused:UNUSED_PAD src0_sel:WORD_1
	v_cvt_f32_f16_e32 v12, v103
	global_store_dwordx4 v[94:95], v[0:3], off
	v_pk_add_f32 v[4:5], v[4:5], v[12:13]
	v_cvt_f32_f16_sdwa v13, v102 dst_sel:DWORD dst_unused:UNUSED_PAD src0_sel:WORD_1
	v_cvt_f32_f16_e32 v12, v102
	v_mov_b32_e32 v102, v1
	v_mov_b32_e32 v103, v5
	v_pk_mul_f32 v[102:103], v[102:103], v[102:103]
	v_pk_add_f32 v[6:7], v[6:7], v[12:13]
	v_mov_b32_e32 v12, v0
	v_mov_b32_e32 v13, v4
	v_pk_fma_f32 v[12:13], v[12:13], v[12:13], v[102:103]
	v_mov_b32_e32 v102, v2
	v_mov_b32_e32 v103, v6
	v_pk_fma_f32 v[12:13], v[102:103], v[102:103], v[12:13]
	v_mov_b32_e32 v102, v3
	v_mov_b32_e32 v103, v7
	v_pk_fma_f32 v[102:103], v[102:103], v[102:103], v[12:13]
	v_cvt_f32_f16_sdwa v13, v101 dst_sel:DWORD dst_unused:UNUSED_PAD src0_sel:WORD_1
	v_cvt_f32_f16_e32 v12, v101
	v_cvt_f32_f16_sdwa v101, v15 dst_sel:DWORD dst_unused:UNUSED_PAD src0_sel:WORD_1
	global_store_dwordx4 v[94:95], v[4:7], off offset:16
	v_pk_add_f32 v[8:9], v[8:9], v[12:13]
	v_cvt_f32_f16_sdwa v13, v100 dst_sel:DWORD dst_unused:UNUSED_PAD src0_sel:WORD_1
	v_cvt_f32_f16_e32 v12, v100
	v_cvt_f32_f16_e32 v100, v15
	v_pk_add_f32 v[10:11], v[10:11], v[12:13]
	v_cvt_f32_f16_sdwa v13, v99 dst_sel:DWORD dst_unused:UNUSED_PAD src0_sel:WORD_1
	v_cvt_f32_f16_e32 v12, v99
	v_pk_add_f32 v[14:15], v[108:109], v[100:101]
	v_mov_b32_e32 v100, v9
	global_store_dwordx4 v[94:95], v[8:11], off offset:32
	v_pk_add_f32 v[12:13], v[106:107], v[12:13]
	global_store_dwordx4 v[94:95], v[12:15], off offset:48
	v_mov_b32_e32 v101, v13
	v_mov_b32_e32 v94, v8
	v_mov_b32_e32 v95, v12
	v_pk_mul_f32 v[100:101], v[100:101], v[100:101]
	v_add_f32_e32 v99, v102, v103
	v_pk_fma_f32 v[94:95], v[94:95], v[94:95], v[100:101]
	v_mov_b32_e32 v100, v10
	v_mov_b32_e32 v101, v14
	v_pk_fma_f32 v[94:95], v[100:101], v[100:101], v[94:95]
	v_mov_b32_e32 v100, v11
	v_mov_b32_e32 v101, v15
	v_pk_fma_f32 v[94:95], v[100:101], v[100:101], v[94:95]
	global_load_dwordx4 v[100:103], v[46:47], off offset:48
	global_load_dwordx4 v[104:107], v[46:47], off offset:32
	global_load_dwordx4 v[108:111], v[46:47], off offset:16
	global_load_dwordx4 v[112:115], v[46:47], off
	v_add_f32_e32 v94, v99, v94
	v_add_f32_e32 v94, v94, v95
	v_mov_b32_e32 v95, v94
	s_nop 1
	v_permlane32_swap_b32 v95, v94
	s_waitcnt lgkmcnt(0)
	v_add_f32_e32 v94, v94, v95
	v_mov_b32_e32 v95, v94
	s_nop 1
	v_permlane16_swap_b32 v95, v94
	s_waitcnt lgkmcnt(0)
	v_add_f32_e32 v94, v94, v95
	s_nop 1
	v_mov_b32_dpp v95, v94 row_ror:8 row_mask:0xf bank_mask:0xf
	s_waitcnt lgkmcnt(0)
	v_add_f32_e32 v94, v94, v95
	s_nop 1
	v_mov_b32_dpp v95, v94 row_half_mirror row_mask:0xf bank_mask:0xf
	s_nop 1
	v_mov_b32_dpp v95, v95 quad_perm:[3,2,1,0] row_mask:0xf bank_mask:0xf
	s_waitcnt lgkmcnt(0)
	v_add_f32_e32 v94, v94, v95
	s_nop 1
	v_mov_b32_dpp v95, v94 quad_perm:[2,3,0,1] row_mask:0xf bank_mask:0xf
	s_waitcnt lgkmcnt(0)
	v_add_f32_e32 v94, v94, v95
	s_nop 1
	v_mov_b32_dpp v95, v94 quad_perm:[1,0,3,2] row_mask:0xf bank_mask:0xf
	s_waitcnt lgkmcnt(0)
	v_add_f32_e32 v94, v94, v95
	v_fmamk_f32 v94, v94, 0x3a800000, v191
	v_cmp_gt_f32_e32 vcc, s12, v94
	v_mul_f32_e32 v95, 0x4b800000, v94
	s_nop 0
	v_cndmask_b32_e32 v94, v94, v95, vcc
	v_rsq_f32_e32 v94, v94
	s_nop 0
	v_mul_f32_e32 v95, 0x45800000, v94
	v_cndmask_b32_e32 v94, v94, v95, vcc
	v_pk_mul_f32 v[0:1], v[0:1], v[94:95] op_sel_hi:[1,0]
	v_pk_mul_f32 v[2:3], v[2:3], v[94:95] op_sel_hi:[1,0]
	s_waitcnt vmcnt(0)
	v_pk_mul_f32 v[0:1], v[112:113], v[0:1]
	v_pk_mul_f32 v[2:3], v[114:115], v[2:3]
	v_cvt_pk_bf16_f32 v0, v0, v1
	v_cvt_pk_bf16_f32 v1, v2, v3
	v_pk_mul_f32 v[2:3], v[4:5], v[94:95] op_sel_hi:[1,0]
	v_pk_mul_f32 v[4:5], v[6:7], v[94:95] op_sel_hi:[1,0]
	v_pk_mul_f32 v[2:3], v[108:109], v[2:3]
	v_pk_mul_f32 v[4:5], v[110:111], v[4:5]
	v_cvt_pk_bf16_f32 v2, v2, v3
	v_cvt_pk_bf16_f32 v3, v4, v5
	v_pk_mul_f32 v[4:5], v[8:9], v[94:95] op_sel_hi:[1,0]
	v_pk_mul_f32 v[6:7], v[10:11], v[94:95] op_sel_hi:[1,0]
	v_pk_mul_f32 v[4:5], v[104:105], v[4:5]
	v_pk_mul_f32 v[6:7], v[6:7], v[106:107]
	v_cvt_pk_bf16_f32 v4, v4, v5
	v_cvt_pk_bf16_f32 v5, v6, v7
	v_pk_mul_f32 v[6:7], v[12:13], v[94:95] op_sel_hi:[1,0]
	v_pk_mul_f32 v[8:9], v[14:15], v[94:95] op_sel_hi:[1,0]
	v_pk_mul_f32 v[6:7], v[6:7], v[100:101]
	v_pk_mul_f32 v[8:9], v[8:9], v[102:103]
	v_cvt_pk_bf16_f32 v6, v6, v7
	v_cvt_pk_bf16_f32 v7, v8, v9
	global_store_dwordx4 v[74:75], v[0:3], off
	global_store_dwordx4 v[74:75], v[4:7], off offset:16
	s_nop 0
	v_mov_b32_e32 v0, v98
	s_andn2_b64 exec, exec, s[8:9]
	s_cbranch_execnz .LBB0_769
